# NSA unit prologue: compressed-K tile loads and rope-table loads batched; top-16 radix-select chain shortened to one VALU-SALU hand-off per bit
# speedup vs baseline: 1.0160x; 1.0096x over previous
; __device__ __forceinline__ float sigmoidf_(float x) { return 1.f / (1.f + __expf(-x)); }
; __device__ __forceinline__ void nsa_ld2(const bf16* base, unsigned off, u32x4& k0, u32x4& k1) { const gcp p = uniform_ptr(base) + off; k0 = gld<u32x4>(p); k1 = gld<u32x4>(p + 16); }
; __device__ __forceinline__ void nsa_unit(const Args& a, LAS unsigned char* lds, int b, int kvh, int qb) {
;     ...
;     { const gcp qp = projU + (prow_off + (unsigned)((PQ + (kvh * 4 + g) * 128 + 8 * h) * 2));
; #pragma unroll
;       for (int ks = 0; ks < 8; ++ks) qf[ks] = gld<bf16x8>(qp + 32 * ks); }
;     float g0, g1, g2; { const gcp gp = projU + (prow_off + (unsigned)((PNG + (kvh * 4 + g) * 3) * 2)); g0 = sigmoidf_(bf1(gld<bf16>(gp))); g1 = sigmoidf_(bf1(gld<bf16>(gp + 2))); g2 = sigmoidf_(bf1(gld<bf16>(gp + 4))); }
;     const int tmax = 64 * qb + 63, ntc = ((((tmax - 31) >> 4) + 1) + 63) >> 6;
;     const int ncv = (t >= 31) ? ((t - 31) >> 4) + 1 : 0;
;     const bf16* kcb = (const bf16*)(a.ws + WS_KCB) + (size_t)((b * 2 + kvh) * 256) * 128; const bf16* vct = (const bf16*)(a.ws + WS_VCT) + (size_t)((b * 2 + kvh) * 128) * 256;
;     __syncthreads();
; #pragma unroll
;     for (int ct = 0; ct < 4; ++ct) if (ct < ntc) { u32x4 k0, k1; nsa_ld2(kcb + (size_t)ct * 64 * 128, offkc, k0, k1); nsa_st_k(lds + ct * NBUF, tid, k0, k1); }
;     __syncthreads();
;     float mx = -1e30f, ls = 0.f;
; #pragma unroll 1
;     for (int ct = 0; ct < ntc; ++ct) { f32x16 s0, s1; nsa_qk(lds + ct * NBUF, qf, r, h, s0, s1);
.LBB0_774:
	s_and_b64 s[0:1], s[2:3], exec
	v_readfirstlane_b32 s71, v0
	s_cselect_b32 s72, s88, s87
	s_lshr_b32 s74, s71, 6
	s_lshl_b32 s73, s74, 3
	v_or_b32_e32 v249, s73, v234
	v_lshl_add_u32 v229, s72, 6, v249
	v_add_u32_e32 v253, s89, v229
	v_mul_lo_u32 v34, v253, s77
	v_add_u32_e32 v35, v33, v34
	global_load_dwordx4 v[126:129], v35, s[28:29]
	global_load_dwordx4 v[130:133], v35, s[28:29] offset:32
	global_load_dwordx4 v[158:161], v35, s[28:29] offset:64
	global_load_dwordx4 v[162:165], v35, s[28:29] offset:96
	global_load_dwordx4 v[166:169], v35, s[28:29] offset:128
	global_load_dwordx4 v[170:173], v35, s[28:29] offset:160
	global_load_dwordx4 v[174:177], v35, s[28:29] offset:192
	global_load_dwordx4 v[178:181], v35, s[28:29] offset:224
	v_add_u32_e32 v34, v42, v34
	global_load_dword v80, v34, s[28:29]
	global_load_ushort v46, v34, s[28:29] offset:4
	s_lshl_b32 s0, s72, 2
	s_addk_i32 s0, 0x42
	s_ashr_i32 s20, s0, 6
	s_cmp_gt_i32 s20, 0
	s_cselect_b64 s[62:63], -1, 0
	s_cmp_lt_i32 s20, 1
	s_cselect_b64 s[4:5], -1, 0
	s_and_b64 vcc, exec, s[62:63]
	s_barrier
	s_cmp_gt_i32 s20, 1
	s_cselect_b64 s[0:1], -1, 0
	s_cmp_gt_i32 s20, 2
	s_cselect_b64 s[16:17], -1, 0
	s_cmp_gt_i32 s20, 3
	s_cselect_b64 s[18:19], -1, 0
	s_cmp_lt_i32 s20, 1
	s_cbranch_scc1 .Lkc_wait_0
	v_lshl_add_u64 v[34:35], s[36:37], 0, v[240:241]
	global_load_dwordx4 v[48:51], v[34:35], off
	global_load_dwordx4 v[52:55], v[34:35], off offset:16
	s_cmp_lt_i32 s20, 2
	s_cbranch_scc1 .Lkc_wait_0
	v_lshl_add_u64 v[34:35], s[40:41], 0, v[240:241]
	global_load_dwordx4 v[56:59], v[34:35], off
	global_load_dwordx4 v[60:63], v[34:35], off offset:16
	s_cmp_lt_i32 s20, 3
	s_cbranch_scc1 .Lkc_wait_0
	v_lshl_add_u64 v[34:35], s[42:43], 0, v[240:241]
	global_load_dwordx4 v[64:67], v[34:35], off
	global_load_dwordx4 v[68:71], v[34:35], off offset:16
	s_cmp_lt_i32 s20, 4
	s_cbranch_scc1 .Lkc_wait_0
	v_lshl_add_u64 v[34:35], s[44:45], 0, v[240:241]
	global_load_dwordx4 v[72:75], v[34:35], off
	global_load_dwordx4 v[76:79], v[34:35], off offset:16
.Lkc_wait_0:
	s_waitcnt vmcnt(0)
	s_cmp_lt_i32 s20, 1
	s_cbranch_scc1 .Lkc_done_0
	ds_write_b128 v242, v[48:51]
	ds_write_b128 v242, v[52:55] offset:16
	s_cmp_lt_i32 s20, 2
	s_cbranch_scc1 .Lkc_done_0
	ds_write_b128 v242, v[56:59] offset:17408
	ds_write_b128 v242, v[60:63] offset:17424
	s_cmp_lt_i32 s20, 3
	s_cbranch_scc1 .Lkc_done_0
	ds_write_b128 v242, v[64:67] offset:34816
	ds_write_b128 v242, v[68:71] offset:34832
	s_cmp_lt_i32 s20, 4
	s_cbranch_scc1 .Lkc_done_0
	ds_write_b128 v242, v[72:75] offset:52224
	ds_write_b128 v242, v[76:79] offset:52240
.Lkc_done_0:
.LBB0_780:
	v_cmp_lt_i32_e64 s[12:13], 30, v229
	s_mov_b64 s[14:15], -1
	s_andn2_b64 vcc, exec, s[4:5]
	v_mbcnt_hi_u32_b32 v84, -1, v243
	s_waitcnt lgkmcnt(0)
	s_barrier
	s_cbranch_vccnz .LBB0_782
	v_mbcnt_hi_u32_b32 v85, -1, v243
	v_and_b32_e32 v34, 64, v85
	v_xor_b32_e32 v83, 32, v85
	v_add_u32_e32 v43, 64, v34
	s_mov_b64 s[14:15], 0

; #define LAS __attribute__((address_space(3)))
; __device__ __forceinline__ void nsa_qk(const LAS unsigned char* kbuf, const bf16x8 (&qf)[8], int r, int h, f32x16& p0, f32x16& p1) {
;     const LAS unsigned char* kp = kbuf + r * NK_ROW + h * 16;
; #pragma unroll
;     for (int i = 0; i < 16; ++i) { p0[i] = 0.f; p1[i] = 0.f; }
;     bf16x8 a0[NSA_QKB], a1[NSA_QKB], b0[NSA_QKB], b1[NSA_QKB];
; #pragma unroll
;     for (int k4 = 0; k4 < NSA_QKB; ++k4) { a0[k4] = *(const LAS bf16x8*)(kp + k4 * 32); a1[k4] = *(const LAS bf16x8*)(kp + 32 * NK_ROW + k4 * 32); }
;     __builtin_amdgcn_sched_barrier(0);
; #pragma unroll
;     for (int kb = 0; kb < 8 / NSA_QKB; kb += 2) {
;         if (kb + 1 < 8 / NSA_QKB) {
; #pragma unroll
;             for (int k4 = 0; k4 < NSA_QKB; ++k4) { b0[k4] = *(const LAS bf16x8*)(kp + (NSA_QKB * (kb + 1) + k4) * 32); b1[k4] = *(const LAS bf16x8*)(kp + 32 * NK_ROW + (NSA_QKB * (kb + 1) + k4) * 32); } }
;         __builtin_amdgcn_sched_barrier(0);
; #pragma unroll
;         for (int k4 = 0; k4 < NSA_QKB; ++k4) { p0 = __builtin_amdgcn_mfma_f32_32x32x16_bf16(a0[k4], qf[NSA_QKB * kb + k4], p0, 0, 0, 0); p1 = __builtin_amdgcn_mfma_f32_32x32x16_bf16(a1[k4], qf[NSA_QKB * kb + k4], p1, 0, 0, 0); }
;         __builtin_amdgcn_sched_barrier(0);
;         if (kb + 2 < 8 / NSA_QKB) {
; #pragma unroll
;             for (int k4 = 0; k4 < NSA_QKB; ++k4) { a0[k4] = *(const LAS bf16x8*)(kp + (NSA_QKB * (kb + 2) + k4) * 32); a1[k4] = *(const LAS bf16x8*)(kp + 32 * NK_ROW + (NSA_QKB * (kb + 2) + k4) * 32); } }
;         __builtin_amdgcn_sched_barrier(0);
;         if (kb + 1 < 8 / NSA_QKB) {
; #pragma unroll
;             for (int k4 = 0; k4 < NSA_QKB; ++k4) { p0 = __builtin_amdgcn_mfma_f32_32x32x16_bf16(b0[k4], qf[NSA_QKB * (kb + 1) + k4], p0, 0, 0, 0); p1 = __builtin_amdgcn_mfma_f32_32x32x16_bf16(b1[k4], qf[NSA_QKB * (kb + 1) + k4], p1, 0, 0, 0); } }
;         __builtin_amdgcn_sched_barrier(0);
;     }
; }
; __device__ __forceinline__ void nsa_unit(const Args& a, LAS unsigned char* lds, int b, int kvh, int qb) {
;     ...
; #pragma unroll 1
;     for (int ct = 0; ct < ntc; ++ct) { f32x16 s0, s1; nsa_qk(lds + ct * NBUF, qf, r, h, s0, s1);
; #pragma unroll
;         for (int i = 0; i < 16; ++i) { const int c0 = 64 * ct + (i & 3) + 8 * (i >> 2) + 4 * h; s0[i] = (c0 < ncv) ? s0[i] : NINF; s1[i] = (c0 + 32 < ncv) ? s1[i] : NINF; }
.LBB0_784:
	v_mov_b32_e32 v89, v48
	ds_read_b128 v[48:51], v86 offset:8704
	ds_read_b128 v[52:55], v86
	ds_read_b128 v[90:93], v86 offset:32
	ds_read_b128 v[94:97], v86 offset:8736
	ds_read_b128 v[98:101], v86 offset:64
	ds_read_b128 v[102:105], v86 offset:96
	ds_read_b128 v[106:109], v86 offset:8768
	ds_read_b128 v[110:113], v86 offset:8800
	s_waitcnt vmcnt(9) lgkmcnt(6)
	v_mfma_f32_32x32x16_bf16 v[64:79], v[52:55], v[126:129], 0
	v_mfma_f32_32x32x16_bf16 v[48:63], v[48:51], v[126:129], 0
	s_waitcnt vmcnt(8) lgkmcnt(4)
	v_mfma_f32_32x32x16_bf16 v[48:63], v[94:97], v[130:133], v[48:63]
	v_mfma_f32_32x32x16_bf16 v[64:79], v[90:93], v[130:133], v[64:79]
	ds_read_b128 v[90:93], v86 offset:8864
	ds_read_b128 v[94:97], v86 offset:8832
	ds_read_b128 v[114:117], v86 offset:128
	ds_read_b128 v[118:121], v86 offset:160
	s_waitcnt vmcnt(7) lgkmcnt(5)
	v_mfma_f32_32x32x16_bf16 v[48:63], v[106:109], v[158:161], v[48:63]
	v_mfma_f32_32x32x16_bf16 v[64:79], v[98:101], v[158:161], v[64:79]
	s_waitcnt vmcnt(6) lgkmcnt(4)
	v_mfma_f32_32x32x16_bf16 v[48:63], v[110:113], v[162:165], v[48:63]
	v_mfma_f32_32x32x16_bf16 v[64:79], v[102:105], v[162:165], v[64:79]
	ds_read_b128 v[98:101], v86 offset:192
	ds_read_b128 v[102:105], v86 offset:224
	ds_read_b128 v[106:109], v86 offset:8896
	ds_read_b128 v[110:113], v86 offset:8928
	s_waitcnt vmcnt(5) lgkmcnt(6)
	v_mfma_f32_32x32x16_bf16 v[48:63], v[94:97], v[166:169], v[48:63]
	s_waitcnt lgkmcnt(5)
	v_mfma_f32_32x32x16_bf16 v[64:79], v[114:117], v[166:169], v[64:79]
	s_waitcnt vmcnt(4)
	v_mfma_f32_32x32x16_bf16 v[48:63], v[90:93], v[170:173], v[48:63]
	s_waitcnt lgkmcnt(4)
	v_mfma_f32_32x32x16_bf16 v[64:79], v[118:121], v[170:173], v[64:79]
	s_waitcnt vmcnt(3) lgkmcnt(1)
	v_mfma_f32_32x32x16_bf16 v[48:63], v[106:109], v[174:177], v[48:63]
	v_mfma_f32_32x32x16_bf16 v[64:79], v[98:101], v[174:177], v[64:79]
	s_waitcnt vmcnt(2) lgkmcnt(0)
	v_mfma_f32_32x32x16_bf16 v[48:63], v[110:113], v[178:181], v[48:63]
	v_mfma_f32_32x32x16_bf16 v[64:79], v[102:105], v[178:181], v[64:79]
	v_subrev_u32_e32 v34, 59, v87
	v_cmp_lt_u32_e32 vcc, v34, v81
	v_subrev_u32_e32 v35, 27, v87
	v_subrev_u32_e32 v36, 58, v87
	s_nop 7
	v_cndmask_b32_e32 v34, v244, v64, vcc
	v_cmp_lt_u32_e32 vcc, v35, v81
	v_subrev_u32_e32 v37, 26, v87
	v_subrev_u32_e32 v38, 57, v87
	v_cndmask_b32_e32 v35, v244, v48, vcc
	v_cmp_lt_u32_e32 vcc, v36, v81
	v_subrev_u32_e32 v39, 25, v87
	v_subrev_u32_e32 v40, 56, v87
	v_cndmask_b32_e32 v36, v244, v65, vcc
	v_cmp_lt_u32_e32 vcc, v37, v81
	v_subrev_u32_e32 v41, 24, v87
	v_subrev_u32_e32 v48, 51, v87
	v_cndmask_b32_e32 v37, v244, v49, vcc
	v_cmp_lt_u32_e32 vcc, v38, v81
	v_subrev_u32_e32 v49, 19, v87
	s_add_i32 s20, s20, -1
	v_cndmask_b32_e32 v38, v244, v66, vcc
	v_cmp_lt_u32_e32 vcc, v39, v81
	v_add_u32_e32 v86, 0x4400, v86
	s_cmp_eq_u32 s20, 0
	v_cndmask_b32_e32 v39, v244, v50, vcc
	v_cmp_lt_u32_e32 vcc, v40, v81
	s_nop 1
	v_cndmask_b32_e32 v40, v244, v67, vcc
	v_cmp_lt_u32_e32 vcc, v41, v81
	s_nop 1
	v_cndmask_b32_e32 v41, v244, v51, vcc
	v_cmp_lt_u32_e32 vcc, v48, v81
	s_nop 1
	v_cndmask_b32_e32 v48, v244, v68, vcc
	v_cmp_lt_u32_e32 vcc, v49, v81
	v_subrev_u32_e32 v49, 50, v87
	s_nop 0
	v_cndmask_b32_e32 v50, v244, v52, vcc
	v_cmp_lt_u32_e32 vcc, v49, v81
	v_subrev_u32_e32 v49, 18, v87
	s_nop 0
	v_cndmask_b32_e32 v51, v244, v69, vcc
	v_cmp_lt_u32_e32 vcc, v49, v81
	v_subrev_u32_e32 v49, 49, v87
	s_nop 0
	v_cndmask_b32_e32 v52, v244, v53, vcc
	v_cmp_lt_u32_e32 vcc, v49, v81
	v_subrev_u32_e32 v49, 17, v87
	s_nop 0
	v_cndmask_b32_e32 v53, v244, v70, vcc
	v_cmp_lt_u32_e32 vcc, v49, v81
	v_subrev_u32_e32 v49, 48, v87
	s_nop 0
	v_cndmask_b32_e32 v54, v244, v54, vcc
	v_cmp_lt_u32_e32 vcc, v49, v81
	v_add_u32_e32 v49, -16, v87
	s_nop 0
	v_cndmask_b32_e32 v64, v244, v71, vcc
	v_cmp_lt_u32_e32 vcc, v49, v81
	v_subrev_u32_e32 v49, 43, v87
	s_nop 0
	v_cndmask_b32_e32 v55, v244, v55, vcc
	v_cmp_lt_u32_e32 vcc, v49, v81
	v_add_u32_e32 v49, -11, v87
	s_nop 0
	v_cndmask_b32_e32 v65, v244, v72, vcc
	v_cmp_lt_u32_e32 vcc, v49, v81
	v_subrev_u32_e32 v49, 42, v87
	s_nop 0
	v_cndmask_b32_e32 v56, v244, v56, vcc
	v_cmp_lt_u32_e32 vcc, v49, v81
	v_add_u32_e32 v49, -10, v87
	s_nop 0
	v_cndmask_b32_e32 v66, v244, v73, vcc
	v_cmp_lt_u32_e32 vcc, v49, v81
	v_subrev_u32_e32 v49, 41, v87
	v_max_f32_e32 v73, v36, v36
	v_cndmask_b32_e32 v57, v244, v57, vcc
	v_cmp_lt_u32_e32 vcc, v49, v81
	v_add_u32_e32 v49, -9, v87
	s_nop 0
	v_cndmask_b32_e32 v67, v244, v74, vcc
	v_cmp_lt_u32_e32 vcc, v49, v81
	v_subrev_u32_e32 v49, 40, v87
	v_max_f32_e32 v74, v38, v38
	v_cndmask_b32_e32 v58, v244, v58, vcc
	v_cmp_lt_u32_e32 vcc, v49, v81
	v_add_u32_e32 v49, -8, v87
	s_nop 0
	v_cndmask_b32_e32 v68, v244, v75, vcc
	v_cmp_lt_u32_e32 vcc, v49, v81
	v_subrev_u32_e32 v49, 35, v87
	v_max_f32_e32 v75, v40, v40
	v_cndmask_b32_e32 v59, v244, v59, vcc
	v_cmp_lt_u32_e32 vcc, v49, v81
	v_add_u32_e32 v49, -3, v87
	s_nop 0
	v_cndmask_b32_e32 v69, v244, v76, vcc
	v_cmp_lt_u32_e32 vcc, v49, v81
	v_subrev_u32_e32 v49, 34, v87
	s_nop 0
	v_cndmask_b32_e32 v60, v244, v60, vcc
	v_cmp_lt_u32_e32 vcc, v49, v81
	v_add_u32_e32 v49, -2, v87
	s_nop 0
	v_cndmask_b32_e32 v70, v244, v77, vcc
	v_cmp_lt_u32_e32 vcc, v49, v81
	v_subrev_u32_e32 v49, 33, v87
	s_nop 0
	v_cndmask_b32_e32 v61, v244, v61, vcc
; __device__ __forceinline__ void nsa_ld2(const bf16* base, unsigned off, u32x4& k0, u32x4& k1) { const gcp p = uniform_ptr(base) + off; k0 = gld<u32x4>(p); k1 = gld<u32x4>(p + 16); }
; __device__ __forceinline__ void nsa_unit(const Args& a, LAS unsigned char* lds, int b, int kvh, int qb) {
;     ...
;     for (int ct = 0; ct < 4; ++ct) if (ct < ntc) { u32x4 k0, k1; nsa_ld2(kcb + (size_t)ct * 64 * 128, offkc, k0, k1); nsa_st_k(lds + ct * NBUF, tid, k0, k1); }
;     ...
;         float tmx = nsa_rowmax(s0, s1); tmx = fmaxf(tmx, __shfl_xor(tmx, 32));
;         const float mnew = fmaxf(mx, tmx), alpha = __builtin_amdgcn_exp2f((mx - mnew) * SM_C), nmc = -mnew * SM_C; mx = mnew;
;         float la = 0.f;
; #pragma unroll
;         for (int i = 0; i < 16; ++i) la += __builtin_amdgcn_exp2f(fmaf(s0[i], SM_C, nmc)) + __builtin_amdgcn_exp2f(fmaf(s1[i], SM_C, nmc));
;         ls = ls * alpha + la; }
	v_cmp_lt_u32_e32 vcc, v49, v81
	v_add_u32_e32 v49, -1, v87
	s_nop 0
	v_cndmask_b32_e32 v71, v244, v78, vcc
	v_cmp_lt_u32_e32 vcc, v49, v81
	v_subrev_u32_e32 v49, 32, v87
	s_nop 0
	v_cndmask_b32_e32 v62, v244, v62, vcc
	v_cmp_lt_u32_e32 vcc, v49, v81
	v_max_f32_e32 v49, v37, v37
	v_max_f32_e32 v49, v73, v49
	v_max_f32_e32 v73, v39, v39
	v_max_f32_e32 v73, v74, v73
	v_max_f32_e32 v74, v41, v41
	v_max3_f32 v49, v34, v35, v49
	v_max_f32_e32 v74, v75, v74
	v_max3_f32 v49, v49, v73, v74
	v_max_f32_e32 v73, v50, v50
	v_max_f32_e32 v74, v48, v48
	v_max_f32_e32 v73, v74, v73
	v_max_f32_e32 v74, v52, v52
	v_max_f32_e32 v75, v51, v51
	v_max_f32_e32 v74, v75, v74
	v_max3_f32 v49, v49, v73, v74
	v_max_f32_e32 v73, v54, v54
	v_max_f32_e32 v74, v53, v53
	v_max_f32_e32 v73, v74, v73
	v_max_f32_e32 v74, v55, v55
	v_max_f32_e32 v75, v64, v64
	v_max_f32_e32 v74, v75, v74
	v_max3_f32 v49, v49, v73, v74
	v_max_f32_e32 v73, v56, v56
	v_max_f32_e32 v74, v65, v65
	v_max_f32_e32 v73, v74, v73
	v_max_f32_e32 v74, v57, v57
	v_max_f32_e32 v75, v66, v66
	v_max_f32_e32 v74, v75, v74
	v_max3_f32 v49, v49, v73, v74
	v_max_f32_e32 v73, v58, v58
	v_max_f32_e32 v74, v67, v67
	v_max_f32_e32 v73, v74, v73
	v_max_f32_e32 v74, v59, v59
	v_max_f32_e32 v75, v68, v68
	v_max_f32_e32 v74, v75, v74
	v_max3_f32 v49, v49, v73, v74
	v_max_f32_e32 v73, v60, v60
	v_max_f32_e32 v74, v69, v69
	v_max_f32_e32 v73, v74, v73
	v_max_f32_e32 v74, v61, v61
	v_max_f32_e32 v75, v70, v70
	v_cndmask_b32_e32 v72, v244, v79, vcc
	v_cmp_lt_u32_e32 vcc, v87, v81
	v_max_f32_e32 v74, v75, v74
	v_max3_f32 v49, v49, v73, v74
	v_cndmask_b32_e32 v63, v244, v63, vcc
	v_max_f32_e32 v73, v62, v62
	v_max_f32_e32 v74, v71, v71
	v_max_f32_e32 v73, v74, v73
	v_max_f32_e32 v74, v63, v63
	v_max_f32_e32 v75, v72, v72
	v_max_f32_e32 v74, v75, v74
	v_max3_f32 v49, v49, v73, v74
	ds_bpermute_b32 v73, v85, v49
	v_add_u32_e32 v87, 64, v87
	s_waitcnt lgkmcnt(0)
	v_max3_f32 v49, v88, v49, v73
	v_mul_f32_e32 v82, 0xbe0293ee, v49
	v_fmamk_f32 v34, v34, 0x3e0293ee, v82
	v_fmamk_f32 v35, v35, 0x3e0293ee, v82
	v_exp_f32_e32 v34, v34
	v_exp_f32_e32 v35, v35
	v_sub_f32_e32 v73, v88, v49
	v_mul_f32_e32 v73, 0x3e0293ee, v73
	v_mov_b32_e32 v88, v49
	v_add_f32_e32 v34, v34, v35
	v_fmamk_f32 v35, v36, 0x3e0293ee, v82
	v_fmamk_f32 v36, v37, 0x3e0293ee, v82
	v_exp_f32_e32 v35, v35
	v_exp_f32_e32 v36, v36
	v_add_f32_e32 v34, 0, v34
	v_add_f32_e32 v35, v35, v36
	v_add_f32_e32 v34, v35, v34
	v_fmamk_f32 v35, v38, 0x3e0293ee, v82
	v_fmamk_f32 v36, v39, 0x3e0293ee, v82
	v_exp_f32_e32 v35, v35
	v_exp_f32_e32 v36, v36
	s_nop 0
	v_add_f32_e32 v35, v35, v36
	v_add_f32_e32 v34, v35, v34
	v_fmamk_f32 v35, v40, 0x3e0293ee, v82
	v_fmamk_f32 v36, v41, 0x3e0293ee, v82
	v_exp_f32_e32 v35, v35
	v_exp_f32_e32 v36, v36
	s_nop 0
	v_add_f32_e32 v35, v35, v36
	v_add_f32_e32 v38, v35, v34
	v_fmamk_f32 v34, v48, 0x3e0293ee, v82
	v_exp_f32_e32 v35, v34
	v_fmamk_f32 v34, v50, 0x3e0293ee, v82
	v_exp_f32_e32 v37, v34
	v_fmamk_f32 v34, v51, 0x3e0293ee, v82
	v_fmamk_f32 v36, v52, 0x3e0293ee, v82
	v_exp_f32_e32 v34, v34
	v_exp_f32_e32 v36, v36
	s_nop 0
	v_pk_add_f32 v[34:35], v[34:35], v[36:37]
	s_nop 0
	v_add_f32_e32 v35, v35, v38
	v_add_f32_e32 v38, v34, v35
	v_fmamk_f32 v34, v53, 0x3e0293ee, v82
	v_exp_f32_e32 v35, v34
	v_fmamk_f32 v34, v54, 0x3e0293ee, v82
	v_exp_f32_e32 v37, v34
	v_fmamk_f32 v34, v64, 0x3e0293ee, v82
	v_fmamk_f32 v36, v55, 0x3e0293ee, v82
	v_exp_f32_e32 v34, v34
	v_exp_f32_e32 v36, v36
	s_nop 0
	v_pk_add_f32 v[34:35], v[34:35], v[36:37]
	s_nop 0
	v_add_f32_e32 v35, v35, v38
	v_add_f32_e32 v38, v34, v35
	v_fmamk_f32 v34, v65, 0x3e0293ee, v82
	v_exp_f32_e32 v35, v34
	v_fmamk_f32 v34, v56, 0x3e0293ee, v82
	v_exp_f32_e32 v37, v34
	v_fmamk_f32 v34, v66, 0x3e0293ee, v82
	v_fmamk_f32 v36, v57, 0x3e0293ee, v82
	v_exp_f32_e32 v34, v34
	v_exp_f32_e32 v36, v36
	s_nop 0
	v_pk_add_f32 v[34:35], v[34:35], v[36:37]
	s_nop 0
	v_add_f32_e32 v35, v35, v38
	v_add_f32_e32 v38, v34, v35
	v_fmamk_f32 v34, v67, 0x3e0293ee, v82
	v_exp_f32_e32 v35, v34
	v_fmamk_f32 v34, v58, 0x3e0293ee, v82
	v_exp_f32_e32 v37, v34
	v_fmamk_f32 v34, v68, 0x3e0293ee, v82
	v_fmamk_f32 v36, v59, 0x3e0293ee, v82
	v_exp_f32_e32 v34, v34
	v_exp_f32_e32 v36, v36
	s_nop 0
	v_pk_add_f32 v[34:35], v[34:35], v[36:37]
	s_nop 0
	v_add_f32_e32 v35, v35, v38
	v_add_f32_e32 v38, v34, v35
	v_fmamk_f32 v34, v69, 0x3e0293ee, v82
	v_exp_f32_e32 v35, v34
	v_fmamk_f32 v34, v60, 0x3e0293ee, v82
	v_exp_f32_e32 v37, v34
	v_fmamk_f32 v34, v70, 0x3e0293ee, v82
	v_fmamk_f32 v36, v61, 0x3e0293ee, v82
	v_exp_f32_e32 v34, v34
	v_exp_f32_e32 v36, v36
	s_nop 0
	v_pk_add_f32 v[34:35], v[34:35], v[36:37]
	s_nop 0
	v_add_f32_e32 v35, v35, v38
	v_add_f32_e32 v38, v34, v35
	v_fmamk_f32 v34, v71, 0x3e0293ee, v82
	v_exp_f32_e32 v35, v34
	v_fmamk_f32 v34, v62, 0x3e0293ee, v82
	v_exp_f32_e32 v37, v34
	v_fmamk_f32 v34, v72, 0x3e0293ee, v82
	v_fmamk_f32 v36, v63, 0x3e0293ee, v82
	v_exp_f32_e32 v34, v34
	v_exp_f32_e32 v36, v36
	s_nop 0
	v_pk_add_f32 v[34:35], v[34:35], v[36:37]
	s_nop 0
	v_add_f32_e32 v35, v35, v38
	v_add_f32_e32 v48, v34, v35
	v_exp_f32_e32 v34, v73
	s_nop 0
	v_fmac_f32_e32 v48, v89, v34
	s_cbranch_scc0 .LBB0_784
	v_mov_b32_e32 v85, v84
	s_branch .LBB0_789
.LBB0_788:
	v_mov_b32_e32 v82, 0x6fce03f9
	v_mov_b32_e32 v48, 0

; __device__ __forceinline__ void nsa_unit(const Args& a, LAS unsigned char* lds, int b, int kvh, int qb) {
;     ...
;     for (int qq = 0; qq < 8; ++qq) {
;         const float imp = impw[qq * 64 + lane] + (lane > 0 ? impw[512 + qq * 64 + lane - 1] : 0.f);
;         const float iv = (lane > qb) ? NINF : ((lane == 0 || lane == qb || lane == qb - 1) ? 1e9f : imp);
;         const unsigned ub = __builtin_bit_cast(unsigned, iv); unsigned key = (ub & 0x80000000u) ? ~ub : (ub | 0x80000000u); key = (key & ~63u) | (unsigned)(63 - lane);
;         unsigned thr = 0u;
; #pragma unroll
;     ...
;         const unsigned long long msk = __ballot(key >= thr);
;         if (lane == 0) { selw[qq * 2] = (unsigned)msk; selw[qq * 2 + 1] = (unsigned)(msk >> 32); }
;     }
.LBB0_869:
	v_add_u32_e32 v34, 0xfffff804, v43
	ds_read_b32 v46, v34
	v_mov_b32_e32 v80, 0
	s_and_saveexec_b64 s[0:1], s[10:11]
	ds_read_b32 v80, v43
	s_or_b64 exec, exec, s[0:1]
	s_waitcnt lgkmcnt(0)
	v_add_f32_e32 v34, v46, v80
	v_mov_b32_e32 v35, 0x4e6e6b28
	v_cndmask_b32_e64 v34, v34, v35, s[20:21]
	v_cndmask_b32_e32 v34, v34, v244, vcc
	v_not_b32_e32 v35, v34
	v_cmp_gt_i32_e64 s[22:23], 0, v34
	s_nop 1
	v_cndmask_b32_e64 v34, -|v34|, v35, s[22:23]
	v_cmp_gt_i32_e64 s[22:23], 0, v34
	s_bcnt1_i32_b64 s24, s[22:23]
	s_cmp_gt_u32 s24, 15
	v_and_b32_e32 v35, 0xffffffc0, v34
	s_cselect_b32 s2, 0x80000000, 0
	v_bitop3_b32 v35, v35, 63, v45 bitop3:0x36
	s_or_b32 s3, s2, 2.0
	v_cmp_le_u32_e64 s[22:23], s3, v35
	s_bcnt1_i32_b64 s24, s[22:23]
	s_cmp_gt_u32 s24, 15
	s_cselect_b32 s2, s3, s2
	s_or_b32 s3, s2, 0x20000000
	v_cmp_le_u32_e64 s[22:23], s3, v35
	s_bcnt1_i32_b64 s24, s[22:23]
	s_cmp_gt_u32 s24, 15
	s_cselect_b32 s2, s3, s2
	s_or_b32 s3, s2, 0x10000000
	v_cmp_le_u32_e64 s[22:23], s3, v35
	s_bcnt1_i32_b64 s24, s[22:23]
	s_cmp_gt_u32 s24, 15
	s_cselect_b32 s2, s3, s2
	s_or_b32 s3, s2, 0x8000000
	v_cmp_le_u32_e64 s[22:23], s3, v35
	s_bcnt1_i32_b64 s24, s[22:23]
	s_cmp_gt_u32 s24, 15
	s_cselect_b32 s2, s3, s2
	s_or_b32 s3, s2, 0x4000000
	v_cmp_le_u32_e64 s[22:23], s3, v35
	s_bcnt1_i32_b64 s24, s[22:23]
	s_cmp_gt_u32 s24, 15
	s_cselect_b32 s2, s3, s2
	s_or_b32 s3, s2, 0x2000000
	v_cmp_le_u32_e64 s[22:23], s3, v35
	s_bcnt1_i32_b64 s24, s[22:23]
	s_cmp_gt_u32 s24, 15
	s_cselect_b32 s2, s3, s2
	s_or_b32 s3, s2, 0x1000000
	v_cmp_le_u32_e64 s[22:23], s3, v35
	s_bcnt1_i32_b64 s24, s[22:23]
	s_cmp_gt_u32 s24, 15
	s_cselect_b32 s2, s3, s2
	s_or_b32 s3, s2, 0x800000
	v_cmp_le_u32_e64 s[22:23], s3, v35
	s_bcnt1_i32_b64 s24, s[22:23]
	s_cmp_gt_u32 s24, 15
	s_cselect_b32 s2, s3, s2
	s_or_b32 s3, s2, 0x400000
	v_cmp_le_u32_e64 s[22:23], s3, v35
	s_bcnt1_i32_b64 s24, s[22:23]
	s_cmp_gt_u32 s24, 15
	s_cselect_b32 s2, s3, s2
	s_or_b32 s3, s2, 0x200000
	v_cmp_le_u32_e64 s[22:23], s3, v35
	s_bcnt1_i32_b64 s24, s[22:23]
	s_cmp_gt_u32 s24, 15
	s_cselect_b32 s2, s3, s2
	s_or_b32 s3, s2, 0x100000
	v_cmp_le_u32_e64 s[22:23], s3, v35
	s_bcnt1_i32_b64 s24, s[22:23]
	s_cmp_gt_u32 s24, 15
	s_cselect_b32 s2, s3, s2
	s_or_b32 s3, s2, 0x80000
	v_cmp_le_u32_e64 s[22:23], s3, v35
	s_bcnt1_i32_b64 s24, s[22:23]
	s_cmp_gt_u32 s24, 15
	s_cselect_b32 s2, s3, s2
	s_or_b32 s3, s2, 0x40000
	v_cmp_le_u32_e64 s[22:23], s3, v35
	s_bcnt1_i32_b64 s24, s[22:23]
	s_cmp_gt_u32 s24, 15
	s_cselect_b32 s2, s3, s2
	s_or_b32 s3, s2, 0x20000
	v_cmp_le_u32_e64 s[22:23], s3, v35
	s_bcnt1_i32_b64 s24, s[22:23]
	s_cmp_gt_u32 s24, 15
	s_cselect_b32 s2, s3, s2
	s_or_b32 s3, s2, 0x10000
	v_cmp_le_u32_e64 s[22:23], s3, v35
	s_bcnt1_i32_b64 s24, s[22:23]
	s_cmp_gt_u32 s24, 15
	s_cselect_b32 s2, s3, s2
	s_or_b32 s3, s2, 0x8000
	v_cmp_le_u32_e64 s[22:23], s3, v35
	s_bcnt1_i32_b64 s24, s[22:23]
	s_cmp_gt_u32 s24, 15
	s_cselect_b32 s2, s3, s2
	s_or_b32 s3, s2, 0x4000
	v_cmp_le_u32_e64 s[22:23], s3, v35
	s_bcnt1_i32_b64 s24, s[22:23]
	s_cmp_gt_u32 s24, 15
	s_cselect_b32 s2, s3, s2
	s_or_b32 s3, s2, 0x2000
	v_cmp_le_u32_e64 s[22:23], s3, v35
	s_bcnt1_i32_b64 s24, s[22:23]
	s_cmp_gt_u32 s24, 15
	s_cselect_b32 s2, s3, s2
	s_or_b32 s3, s2, 0x1000
	v_cmp_le_u32_e64 s[22:23], s3, v35
	s_bcnt1_i32_b64 s24, s[22:23]
	s_cmp_gt_u32 s24, 15
	s_cselect_b32 s2, s3, s2
	s_or_b32 s3, s2, 0x800
	v_cmp_le_u32_e64 s[22:23], s3, v35
	s_bcnt1_i32_b64 s24, s[22:23]
	s_cmp_gt_u32 s24, 15
	s_cselect_b32 s2, s3, s2
	s_or_b32 s3, s2, 0x400
	v_cmp_le_u32_e64 s[22:23], s3, v35
	s_bcnt1_i32_b64 s24, s[22:23]
	s_cmp_gt_u32 s24, 15
	s_cselect_b32 s2, s3, s2
	s_or_b32 s3, s2, 0x200
	v_cmp_le_u32_e64 s[22:23], s3, v35
	s_bcnt1_i32_b64 s24, s[22:23]
	s_cmp_gt_u32 s24, 15
	s_cselect_b32 s2, s3, s2
	s_or_b32 s3, s2, 0x100
	v_cmp_le_u32_e64 s[22:23], s3, v35
	s_bcnt1_i32_b64 s24, s[22:23]
	s_cmp_gt_u32 s24, 15
	s_cselect_b32 s2, s3, s2
	s_or_b32 s3, s2, 0x80
	v_cmp_le_u32_e64 s[22:23], s3, v35
	s_bcnt1_i32_b64 s24, s[22:23]
	s_cmp_gt_u32 s24, 15
	s_cselect_b32 s2, s3, s2
	s_or_b32 s3, s2, 64
	v_cmp_le_u32_e64 s[22:23], s3, v35
	s_bcnt1_i32_b64 s24, s[22:23]
	s_cmp_gt_u32 s24, 15
	s_cselect_b32 s2, s3, s2
	s_or_b32 s3, s2, 32
	v_cmp_le_u32_e64 s[22:23], s3, v35
	s_bcnt1_i32_b64 s24, s[22:23]
	s_cmp_gt_u32 s24, 15
	s_cselect_b32 s2, s3, s2
	s_or_b32 s3, s2, 16
	v_cmp_le_u32_e64 s[22:23], s3, v35
	s_bcnt1_i32_b64 s24, s[22:23]
	s_cmp_gt_u32 s24, 15
	s_cselect_b32 s2, s3, s2
	s_or_b32 s3, s2, 8
	v_cmp_le_u32_e64 s[22:23], s3, v35
	s_bcnt1_i32_b64 s24, s[22:23]
	s_cmp_gt_u32 s24, 15
	s_cselect_b32 s2, s3, s2
	s_or_b32 s3, s2, 4
	v_cmp_le_u32_e64 s[22:23], s3, v35
	s_bcnt1_i32_b64 s24, s[22:23]
	s_cmp_gt_u32 s24, 15
	s_cselect_b32 s2, s3, s2
	s_or_b32 s3, s2, 2
	v_cmp_le_u32_e64 s[22:23], s3, v35
	s_bcnt1_i32_b64 s24, s[22:23]
	s_cmp_gt_u32 s24, 15
	s_cselect_b32 s2, s3, s2
	s_or_b32 s3, s2, 1
	v_cmp_le_u32_e64 s[22:23], s3, v35
	s_bcnt1_i32_b64 s24, s[22:23]
	s_cmp_gt_u32 s24, 15
	s_cselect_b32 s0, s3, s2
	v_cmp_le_u32_e64 s[2:3], s0, v35
	s_and_saveexec_b64 s[0:1], s[8:9]
	s_cbranch_execz .LBB0_868
	s_add_i32 s22, s33, s4
	v_mov_b32_e32 v34, s22
	v_mov_b64_e32 v[36:37], s[2:3]
	ds_write_b64 v34, v[36:37]
	s_branch .LBB0_868

; #define GAS __attribute__((address_space(1)))
; __device__ __forceinline__ unsigned cvt_pk_bf16(float lo, float hi) { unsigned r; asm volatile("v_cvt_pk_bf16_f32 %0, %1, %2" : "=v"(r) : "v"(lo), "v"(hi)); return r; }
; __device__ __forceinline__ gcp uniform_ptr(const void* p) { const unsigned long long v = (unsigned long long)p; const unsigned lo = __builtin_amdgcn_readfirstlane((unsigned)v), hi = __builtin_amdgcn_readfirstlane((unsigned)(v >> 32)); return (gcp)(((unsigned long long)hi << 32) | lo); }
; __device__ __forceinline__ void nsa_unit(const Args& a, LAS unsigned char* lds, int b, int kvh, int qb) {
;     ...
;     GAS unsigned char* mp = (GAS unsigned char*)uniform_ptr(a.ws + WS_MIX) + ((unsigned)m * 4096u + (unsigned)(((kvh * 4 + g) * 128 + 4 * h) * 2));
; #pragma unroll
;     for (int dt = 0; dt < 4; ++dt)
; #pragma unroll
;         for (int aa = 0; aa < 4; ++aa) { u32x2 wv; wv.x = pg8::cvt_pk_bf16(o[dt][4 * aa] * g0, o[dt][4 * aa + 1] * g0); wv.y = pg8::cvt_pk_bf16(o[dt][4 * aa + 2] * g0, o[dt][4 * aa + 3] * g0); *(GAS u32x2*)(mp + (32 * dt + 8 * aa) * 2) = wv; }
;     { const gcp rpb = uniform_ptr(a.ws + WS_ROPE) + (unsigned)((t * 32 + 8 * h) * 4);
;       u32x4 w0 = __builtin_bit_cast(u32x4, qf[0]), w1 = __builtin_bit_cast(u32x4, qf[1]);
; #pragma unroll
;       for (int jj = 0; jj < 4; ++jj) { const float c0 = gld<float>(rpb + 8 * jj), c1 = gld<float>(rpb + 8 * jj + 4), s0 = gld<float>(rpb + 64 + 8 * jj), s1 = gld<float>(rpb + 64 + 8 * jj + 4);
;           const float xa0 = bflo(w0[jj]), xa1 = bfhi(w0[jj]), xb0 = bflo(w1[jj]), xb1 = bfhi(w1[jj]);
;           w0[jj] = pg8::cvt_pk_bf16(xa0 * c0 - xb0 * s0, xa1 * c1 - xb1 * s1); w1[jj] = pg8::cvt_pk_bf16(xb0 * c0 + xa0 * s0, xb1 * c1 + xa1 * s1); }
;       qf[0] = __builtin_bit_cast(bf16x8, w0); qf[1] = __builtin_bit_cast(bf16x8, w1); }
;     const int nS = qb + 1, jlo = qb > 8 ? qb - 8 : 0, nTot = nS + (qb - jlo + 1);
;     const bf16* ksb = proj + (size_t)b * T * PW + PKS + kvh * 128; const bf16* kwb = proj + (size_t)b * T * PW + PKW + kvh * 128;
;     const bf16* vsb = (const bf16*)(a.ws + WS_VTS) + (size_t)((b * 2 + kvh) * 128) * VTP; const bf16* vwb = (const bf16*)(a.ws + WS_VTW) + (size_t)((b * 2 + kvh) * 128) * VTP;
.LBB0_890:
	v_add_f32_e32 v34, 1.0, v254
	v_div_scale_f32 v35, s[0:1], v34, v34, 1.0
	v_rcp_f32_e32 v36, v35
	v_lshl_or_b32 v48, v253, 12, v248
	s_add_i32 s14, s72, 1
	s_not_b32 s2, s72
	v_fma_f32 v37, -v35, v36, 1.0
	v_fmac_f32_e32 v36, v37, v36
	v_div_scale_f32 v37, vcc, 1.0, v34, 1.0
	v_mul_f32_e32 v38, v37, v36
	v_fma_f32 v39, -v35, v38, v37
	v_fmac_f32_e32 v38, v39, v36
	v_fma_f32 v35, -v35, v38, v37
	v_div_fmas_f32 v35, v35, v36, v38
	v_div_fixup_f32 v36, v35, v34, 1.0
	v_mul_f32_e32 v34, v36, v110
	v_mul_f32_e32 v35, v36, v111
	v_cvt_pk_bf16_f32 v34, v34, v35
	v_mul_f32_e32 v35, v36, v112
	v_mul_f32_e32 v37, v36, v113
	v_cvt_pk_bf16_f32 v35, v35, v37
	global_store_dwordx2 v48, v[34:35], s[30:31]
	v_mul_f32_e32 v34, v36, v114
	v_mul_f32_e32 v35, v36, v115
	v_cvt_pk_bf16_f32 v34, v34, v35
	v_mul_f32_e32 v35, v36, v116
	v_mul_f32_e32 v37, v36, v117
	v_cvt_pk_bf16_f32 v35, v35, v37
	global_store_dwordx2 v48, v[34:35], s[30:31] offset:16
	v_mul_f32_e32 v34, v36, v118
	v_mul_f32_e32 v35, v36, v119
	v_cvt_pk_bf16_f32 v34, v34, v35
	v_mul_f32_e32 v35, v36, v120
	v_mul_f32_e32 v37, v36, v121
	v_cvt_pk_bf16_f32 v35, v35, v37
	global_store_dwordx2 v48, v[34:35], s[30:31] offset:32
	v_mul_f32_e32 v34, v36, v122
	v_mul_f32_e32 v35, v36, v123
	v_cvt_pk_bf16_f32 v34, v34, v35
	v_mul_f32_e32 v35, v36, v124
	v_mul_f32_e32 v37, v36, v125
	v_cvt_pk_bf16_f32 v35, v35, v37
	global_store_dwordx2 v48, v[34:35], s[30:31] offset:48
	v_mul_f32_e32 v34, v36, v94
	v_mul_f32_e32 v35, v36, v95
	v_cvt_pk_bf16_f32 v34, v34, v35
	v_mul_f32_e32 v35, v36, v96
	v_mul_f32_e32 v37, v36, v97
	v_cvt_pk_bf16_f32 v35, v35, v37
	global_store_dwordx2 v48, v[34:35], s[30:31] offset:64
	v_mul_f32_e32 v34, v36, v98
	v_mul_f32_e32 v35, v36, v99
	v_cvt_pk_bf16_f32 v34, v34, v35
	v_mul_f32_e32 v35, v36, v100
	v_mul_f32_e32 v37, v36, v101
	v_cvt_pk_bf16_f32 v35, v35, v37
	global_store_dwordx2 v48, v[34:35], s[30:31] offset:80
	v_mul_f32_e32 v34, v36, v102
	v_mul_f32_e32 v35, v36, v103
	v_cvt_pk_bf16_f32 v34, v34, v35
	v_mul_f32_e32 v35, v36, v104
	v_mul_f32_e32 v37, v36, v105
	v_cvt_pk_bf16_f32 v35, v35, v37
	global_store_dwordx2 v48, v[34:35], s[30:31] offset:96
	v_mul_f32_e32 v34, v36, v106
	v_mul_f32_e32 v35, v36, v107
	v_cvt_pk_bf16_f32 v34, v34, v35
	v_mul_f32_e32 v35, v36, v108
	v_mul_f32_e32 v37, v36, v109
	v_cvt_pk_bf16_f32 v35, v35, v37
	global_store_dwordx2 v48, v[34:35], s[30:31] offset:112
	v_mul_f32_e32 v34, v36, v78
	v_mul_f32_e32 v35, v36, v79
	v_cvt_pk_bf16_f32 v34, v34, v35
	v_mul_f32_e32 v35, v36, v80
	v_mul_f32_e32 v37, v36, v81
	v_cvt_pk_bf16_f32 v35, v35, v37
	global_store_dwordx2 v48, v[34:35], s[30:31] offset:128
	v_mul_f32_e32 v34, v36, v82
	v_mul_f32_e32 v35, v36, v83
	v_cvt_pk_bf16_f32 v34, v34, v35
	v_mul_f32_e32 v35, v36, v84
	v_mul_f32_e32 v37, v36, v85
	v_cvt_pk_bf16_f32 v35, v35, v37
	global_store_dwordx2 v48, v[34:35], s[30:31] offset:144
	v_mul_f32_e32 v34, v36, v86
	v_mul_f32_e32 v35, v36, v87
	v_cvt_pk_bf16_f32 v34, v34, v35
	v_mul_f32_e32 v35, v36, v88
	v_mul_f32_e32 v37, v36, v89
	v_cvt_pk_bf16_f32 v35, v35, v37
	global_store_dwordx2 v48, v[34:35], s[30:31] offset:160
	v_mul_f32_e32 v34, v36, v90
	v_mul_f32_e32 v35, v36, v91
	v_cvt_pk_bf16_f32 v34, v34, v35
	v_mul_f32_e32 v35, v36, v92
	v_mul_f32_e32 v37, v36, v93
	v_cvt_pk_bf16_f32 v35, v35, v37
	global_store_dwordx2 v48, v[34:35], s[30:31] offset:176
	v_mul_f32_e32 v34, v36, v62
	v_mul_f32_e32 v35, v36, v63
	v_cvt_pk_bf16_f32 v34, v34, v35
	v_mul_f32_e32 v35, v36, v64
	v_mul_f32_e32 v37, v36, v65
	v_cvt_pk_bf16_f32 v35, v35, v37
	global_store_dwordx2 v48, v[34:35], s[30:31] offset:192
	v_mul_f32_e32 v34, v36, v66
	v_mul_f32_e32 v35, v36, v67
	v_cvt_pk_bf16_f32 v34, v34, v35
	v_mul_f32_e32 v35, v36, v68
	v_mul_f32_e32 v37, v36, v69
	v_cvt_pk_bf16_f32 v35, v35, v37
	global_store_dwordx2 v48, v[34:35], s[30:31] offset:208
	v_mul_f32_e32 v34, v36, v70
	v_mul_f32_e32 v35, v36, v71
	v_cvt_pk_bf16_f32 v34, v34, v35
	v_mul_f32_e32 v35, v36, v72
	v_mul_f32_e32 v37, v36, v73
	v_cvt_pk_bf16_f32 v35, v35, v37
	global_store_dwordx2 v48, v[34:35], s[30:31] offset:224
	v_mul_f32_e32 v34, v36, v74
	v_mul_f32_e32 v35, v36, v75
	v_cvt_pk_bf16_f32 v34, v34, v35
	v_mul_f32_e32 v35, v36, v76
	v_mul_f32_e32 v36, v36, v77
	v_cvt_pk_bf16_f32 v35, v35, v36
	global_store_dwordx2 v48, v[34:35], s[30:31] offset:240
	v_and_b32_e32 v34, 32, v0
	v_lshl_or_b32 v43, v229, 7, v34
	global_load_dwordx2 v[34:35], v43, s[34:35]
	global_load_dwordx2 v[36:37], v43, s[34:35] offset:64
	global_load_dwordx2 v[98:99], v43, s[34:35] offset:8
	global_load_dwordx2 v[100:101], v43, s[34:35] offset:72
	global_load_dwordx2 v[102:103], v43, s[34:35] offset:16
	global_load_dwordx2 v[104:105], v43, s[34:35] offset:80
	global_load_dwordx2 v[106:107], v43, s[34:35] offset:24
	global_load_dwordx2 v[108:109], v43, s[34:35] offset:88
	v_lshlrev_b32_e32 v39, 16, v126
	v_lshlrev_b32_e32 v38, 16, v130
	s_add_i32 s0, s72, -8
	s_cmp_gt_i32 s72, 8
	s_cselect_b32 s4, s0, 0
	s_sub_i32 s15, s72, s4
	s_add_i32 s15, s15, s14
	s_cmp_gt_i32 s72, -1
	s_cselect_b64 s[0:1], -1, 0
	s_add_i32 s16, s4, s2
	s_and_b64 s[2:3], s[0:1], exec
	s_cselect_b32 s5, s91, s95
	s_cselect_b32 s17, s90, s94
	s_lshl_b32 s12, s16, 6
	s_and_b64 s[2:3], s[0:1], exec
	s_cselect_b32 s12, 0, s12
	s_ashr_i32 s13, s12, 31
	s_mul_i32 s2, s12, 0x2e00
	s_mul_hi_i32 s3, s12, 0x2e00
	s_add_u32 s2, s17, s2
	s_addc_u32 s3, s5, s3
	s_and_b64 s[0:1], s[0:1], exec
	s_cselect_b32 s5, s97, s70
	s_cselect_b32 s17, s96, s69
	s_lshl_b64 s[0:1], s[12:13], 1
	s_add_u32 s0, s17, s0
	s_addc_u32 s1, s5, s1
	s_lshl_b32 s5, s74, 1
	s_or_b32 s5, s5, 1
	s_lshl_b32 s17, s74, 11
	s_lshl_b32 s19, s5, 2
	s_add_i32 s18, s17, 0
	v_mov_b32_e32 v51, v47
	s_lshl_b32 s20, s5, 10
	s_lshl_b32 s21, s74, 4
	v_or_b32_e32 v54, s21, v235
	s_lshl_b32 s22, s5, 3
	v_or_b32_e32 v55, s22, v235
	v_mov_b32_e32 v53, v47
	s_waitcnt vmcnt(7)
; __device__ __forceinline__ unsigned cvt_pk_bf16(float lo, float hi) { unsigned r; asm volatile("v_cvt_pk_bf16_f32 %0, %1, %2" : "=v"(r) : "v"(lo), "v"(hi)); return r; }
; __device__ __forceinline__ gcp uniform_ptr(const void* p) { const unsigned long long v = (unsigned long long)p; const unsigned lo = __builtin_amdgcn_readfirstlane((unsigned)v), hi = __builtin_amdgcn_readfirstlane((unsigned)(v >> 32)); return (gcp)(((unsigned long long)hi << 32) | lo); }
; __device__ __forceinline__ void nsa_unit(const Args& a, LAS unsigned char* lds, int b, int kvh, int qb) {
;     ...
;     { const gcp rpb = uniform_ptr(a.ws + WS_ROPE) + (unsigned)((t * 32 + 8 * h) * 4);
;       u32x4 w0 = __builtin_bit_cast(u32x4, qf[0]), w1 = __builtin_bit_cast(u32x4, qf[1]);
; #pragma unroll
;       for (int jj = 0; jj < 4; ++jj) { const float c0 = gld<float>(rpb + 8 * jj), c1 = gld<float>(rpb + 8 * jj + 4), s0 = gld<float>(rpb + 64 + 8 * jj), s1 = gld<float>(rpb + 64 + 8 * jj + 4);
;           const float xa0 = bflo(w0[jj]), xa1 = bfhi(w0[jj]), xb0 = bflo(w1[jj]), xb1 = bfhi(w1[jj]);
;           w0[jj] = pg8::cvt_pk_bf16(xa0 * c0 - xb0 * s0, xa1 * c1 - xb1 * s1); w1[jj] = pg8::cvt_pk_bf16(xb0 * c0 + xa0 * s0, xb1 * c1 + xa1 * s1); }
;       qf[0] = __builtin_bit_cast(bf16x8, w0); qf[1] = __builtin_bit_cast(bf16x8, w1); }
;     const int nS = qb + 1, jlo = qb > 8 ? qb - 8 : 0, nTot = nS + (qb - jlo + 1);
;     const bf16* ksb = proj + (size_t)b * T * PW + PKS + kvh * 128; const bf16* kwb = proj + (size_t)b * T * PW + PKW + kvh * 128;
;     const bf16* vsb = (const bf16*)(a.ws + WS_VTS) + (size_t)((b * 2 + kvh) * 128) * VTP; const bf16* vwb = (const bf16*)(a.ws + WS_VTW) + (size_t)((b * 2 + kvh) * 128) * VTP;
;     ...
;     const unsigned ldsb = (unsigned)(size_t)lds;
;     constexpr int KRING = 3, VOFF = KRING * NTB;
;     auto tile_src = [&](int i2, const bf16*& kt, const bf16*& vt) { if (i2 < nS) { kt = ksb + (size_t)(64 * i2) * PW; vt = vsb + 64 * i2; } else { const int j = jlo + i2 - nS; kt = kwb + (size_t)(64 * j) * PW; vt = vwb + 64 * j; } };
;     __syncthreads();
;     { const bf16 *kt, *vt; tile_src(0, kt, vt); nsa_dma_tile(kt, PW * 2, vt, VTP * 2, ldsb, ldsb + VOFF, w, lane);
;       if (nTot > 1) { tile_src(1, kt, vt); nsa_dma_tile(kt, PW * 2, vt, VTP * 2, ldsb + NTB, ldsb + VOFF + NTB, w, lane); } }
	v_mov_b32_e32 v41, v34
	s_waitcnt vmcnt(6)
	v_mov_b32_e32 v40, v36
	v_pk_mul_f32 v[40:41], v[40:41], v[38:39]
	s_nop 0
	v_sub_f32_e32 v46, v41, v40
	v_mov_b32_e32 v40, v34
	v_mov_b32_e32 v41, v36
	v_pk_mul_f32 v[38:39], v[40:41], v[38:39]
	v_mov_b32_e32 v34, v37
	v_add_f32_e32 v49, v38, v39
	v_and_b32_e32 v39, 0xffff0000, v126
	v_and_b32_e32 v38, 0xffff0000, v130
	v_pk_mul_f32 v[40:41], v[34:35], v[38:39]
	v_mov_b32_e32 v36, v35
	v_sub_f32_e32 v34, v41, v40
	v_cvt_pk_bf16_f32 v182, v46, v34
	v_pk_mul_f32 v[34:35], v[36:37], v[38:39]
	v_lshlrev_b32_e32 v39, 16, v127
	v_add_f32_e32 v34, v34, v35
	v_cvt_pk_bf16_f32 v186, v49, v34
	s_waitcnt vmcnt(4)
	v_mov_b32_e32 v34, v98
	v_mov_b32_e32 v35, v99
	v_mov_b32_e32 v36, v100
	v_mov_b32_e32 v37, v101
	v_lshlrev_b32_e32 v38, 16, v131
	v_mov_b32_e32 v41, v34
	v_mov_b32_e32 v40, v36
	v_pk_mul_f32 v[40:41], v[40:41], v[38:39]
	s_nop 0
	v_sub_f32_e32 v46, v41, v40
	v_mov_b32_e32 v40, v34
	v_mov_b32_e32 v41, v36
	v_pk_mul_f32 v[38:39], v[40:41], v[38:39]
	v_mov_b32_e32 v34, v37
	v_add_f32_e32 v49, v38, v39
	v_and_b32_e32 v39, 0xffff0000, v127
	v_and_b32_e32 v38, 0xffff0000, v131
	v_pk_mul_f32 v[40:41], v[34:35], v[38:39]
	v_mov_b32_e32 v36, v35
	v_sub_f32_e32 v34, v41, v40
	v_cvt_pk_bf16_f32 v183, v46, v34
	v_pk_mul_f32 v[34:35], v[36:37], v[38:39]
	v_lshlrev_b32_e32 v39, 16, v128
	v_add_f32_e32 v34, v34, v35
	v_cvt_pk_bf16_f32 v187, v49, v34
	s_waitcnt vmcnt(2)
	v_mov_b32_e32 v34, v102
	v_mov_b32_e32 v35, v103
	v_mov_b32_e32 v36, v104
	v_mov_b32_e32 v37, v105
	v_lshlrev_b32_e32 v38, 16, v132
	v_mov_b32_e32 v41, v34
	v_mov_b32_e32 v40, v36
	v_pk_mul_f32 v[40:41], v[40:41], v[38:39]
	s_nop 0
	v_sub_f32_e32 v46, v41, v40
	v_mov_b32_e32 v40, v34
	v_mov_b32_e32 v41, v36
	v_pk_mul_f32 v[38:39], v[40:41], v[38:39]
	v_mov_b32_e32 v34, v37
	v_add_f32_e32 v49, v38, v39
	v_and_b32_e32 v39, 0xffff0000, v128
	v_and_b32_e32 v38, 0xffff0000, v132
	v_pk_mul_f32 v[40:41], v[34:35], v[38:39]
	v_mov_b32_e32 v36, v35
	v_sub_f32_e32 v34, v41, v40
	v_cvt_pk_bf16_f32 v184, v46, v34
	v_pk_mul_f32 v[34:35], v[36:37], v[38:39]
	v_lshlrev_b32_e32 v39, 16, v129
	v_add_f32_e32 v34, v34, v35
	v_cvt_pk_bf16_f32 v188, v49, v34
	s_waitcnt vmcnt(0)
	v_mov_b32_e32 v34, v106
	v_mov_b32_e32 v35, v107
	v_mov_b32_e32 v36, v108
	v_mov_b32_e32 v37, v109
	v_lshlrev_b32_e32 v38, 16, v133
	v_or_b32_e32 v49, s19, v239
	v_mov_b32_e32 v41, v34
	v_mov_b32_e32 v40, v36
	v_pk_mul_f32 v[40:41], v[40:41], v[38:39]
	s_nop 0
	v_sub_f32_e32 v43, v41, v40
	v_mov_b32_e32 v40, v34
	v_mov_b32_e32 v41, v36
	v_pk_mul_f32 v[38:39], v[40:41], v[38:39]
	v_mov_b32_e32 v34, v37
	v_add_f32_e32 v46, v38, v39
	v_and_b32_e32 v39, 0xffff0000, v129
	v_and_b32_e32 v38, 0xffff0000, v133
	v_pk_mul_f32 v[40:41], v[34:35], v[38:39]
	v_mov_b32_e32 v36, v35
	v_sub_f32_e32 v34, v41, v40
	v_cvt_pk_bf16_f32 v185, v43, v34
	v_pk_mul_f32 v[34:35], v[36:37], v[38:39]
	v_or_b32_e32 v43, s73, v239
	v_add_f32_e32 v34, v34, v35
	v_cvt_pk_bf16_f32 v189, v46, v34
	v_bitop3_b32 v34, s73, v0, v239 bitop3:0x36
	v_lshlrev_b32_e32 v34, 4, v34
	v_and_b32_e32 v46, 0xf0, v34
	v_mov_b64_e32 v[34:35], s[2:3]
	v_mad_u64_u32 v[36:37], s[2:3], v43, s77, v[34:35]
	v_lshl_add_u64 v[36:37], v[36:37], 0, v[46:47]
	s_barrier
	s_mov_b32 s2, m0
	s_mov_b32 m0, s18
	s_nop 0
	global_load_lds_dwordx4 v[36:37], off
	s_mov_b32 m0, s2
	v_bitop3_b32 v36, s19, v0, v239 bitop3:0x36
	v_lshlrev_b32_e32 v36, 4, v36
	v_and_b32_e32 v50, 0xf0, v36
	v_mad_u64_u32 v[34:35], s[2:3], v49, s77, v[34:35]
	v_lshl_add_u64 v[34:35], v[34:35], 0, v[50:51]
	s_add_i32 s2, s20, 0
	s_mov_b32 s3, m0
	s_mov_b32 m0, s2
	s_nop 0
	global_load_lds_dwordx4 v[34:35], off
	s_mov_b32 m0, s3
	v_mov_b64_e32 v[34:35], s[0:1]
	v_mad_u64_u32 v[36:37], s[0:1], v54, s78, v[34:35]
	v_lshl_add_u64 v[36:37], v[36:37], 0, v[226:227]
	s_add_i32 s0, s17, s79
	s_mov_b32 s1, m0
	s_mov_b32 m0, s0
	s_nop 0
	global_load_lds_dwordx4 v[36:37], off
	s_mov_b32 m0, s1
	v_lshrrev_b32_e32 v36, 1, v55
	v_xor_b32_e32 v36, v36, v0
	v_lshlrev_b32_e32 v36, 4, v36
	v_and_b32_e32 v52, 0x70, v36
	v_mad_u64_u32 v[34:35], s[0:1], v55, s78, v[34:35]
	v_lshl_add_u64 v[34:35], v[34:35], 0, v[52:53]
	s_add_i32 s0, s20, s79
	s_mov_b32 s1, m0
	s_mov_b32 m0, s0
	s_nop 0
	global_load_lds_dwordx4 v[34:35], off
	s_mov_b32 m0, s1
	s_cmp_lt_i32 s15, 1
	s_cbranch_scc1 .LBB0_892
	v_mad_u64_u32 v[34:35], s[0:1], v43, s77, 0
	v_mad_u64_u32 v[36:37], s[0:1], v49, s77, 0
	v_mad_u64_u32 v[38:39], s[0:1], v54, s78, 0
	v_mad_u64_u32 v[40:41], s[0:1], v55, s78, 0
	s_cmp_gt_i32 s72, 0
	s_cselect_b64 s[0:1], -1, 0
	s_sub_i32 s4, s4, s72
	s_and_b64 s[2:3], s[0:1], exec
	s_cselect_b32 s5, s91, s95
	s_cselect_b32 s12, s90, s94
	s_lshl_b32 s4, s4, 6
	s_and_b64 s[2:3], s[0:1], exec
	s_cselect_b32 s2, 64, s4
	s_ashr_i32 s3, s2, 31
	s_mul_i32 s4, s2, 0x2e00
	s_mul_hi_i32 s13, s2, 0x2e00
	s_add_u32 s4, s12, s4
	s_addc_u32 s5, s5, s13
	s_and_b64 s[0:1], s[0:1], exec
	s_cselect_b32 s12, s97, s70
	s_cselect_b32 s13, s96, s69
	s_lshl_b64 s[0:1], s[2:3], 1
	s_add_u32 s0, s13, s0
	v_lshl_add_u64 v[34:35], s[4:5], 0, v[34:35]
	s_addc_u32 s1, s12, s1
	v_lshl_add_u64 v[34:35], v[34:35], 0, v[46:47]
	s_add_i32 s2, 0, 0x4000
	s_add_i32 s3, s17, s2
	s_mov_b32 s12, m0
	s_mov_b32 m0, s3
	s_nop 0
	global_load_lds_dwordx4 v[34:35], off
	s_mov_b32 m0, s12
	v_lshl_add_u64 v[34:35], s[4:5], 0, v[36:37]
	v_lshl_add_u64 v[34:35], v[34:35], 0, v[50:51]
	s_add_i32 s2, s20, s2
	s_mov_b32 s3, m0
	s_mov_b32 m0, s2
	s_nop 0
	global_load_lds_dwordx4 v[34:35], off
	s_mov_b32 m0, s3
	v_lshl_add_u64 v[34:35], s[0:1], 0, v[38:39]
	v_lshl_add_u64 v[34:35], v[34:35], 0, v[226:227]
	s_add_i32 s2, 0, 0x10000
	s_add_i32 s3, s17, s2
	s_mov_b32 s4, m0
	s_mov_b32 m0, s3
	s_nop 0
	global_load_lds_dwordx4 v[34:35], off
	s_mov_b32 m0, s4
	v_lshl_add_u64 v[34:35], s[0:1], 0, v[40:41]
	v_lshl_add_u64 v[34:35], v[34:35], 0, v[52:53]
	s_add_i32 s0, s20, s2
	s_mov_b32 s1, m0
	s_mov_b32 m0, s0
	s_nop 0
	global_load_lds_dwordx4 v[34:35], off
	s_mov_b32 m0, s1

; __device__ __forceinline__ float sigmoidf_(float x) { return 1.f / (1.f + __expf(-x)); }
; __device__ __forceinline__ void nsa_ld2(const bf16* base, unsigned off, u32x4& k0, u32x4& k1) { const gcp p = uniform_ptr(base) + off; k0 = gld<u32x4>(p); k1 = gld<u32x4>(p + 16); }
; __device__ __forceinline__ void nsa_unit(const Args& a, LAS unsigned char* lds, int b, int kvh, int qb) {
;     ...
;     { const gcp qp = projU + (prow_off + (unsigned)((PQ + (kvh * 4 + g) * 128 + 8 * h) * 2));
; #pragma unroll
;       for (int ks = 0; ks < 8; ++ks) qf[ks] = gld<bf16x8>(qp + 32 * ks); }
;     float g0, g1, g2; { const gcp gp = projU + (prow_off + (unsigned)((PNG + (kvh * 4 + g) * 3) * 2)); g0 = sigmoidf_(bf1(gld<bf16>(gp))); g1 = sigmoidf_(bf1(gld<bf16>(gp + 2))); g2 = sigmoidf_(bf1(gld<bf16>(gp + 4))); }
;     const int tmax = 64 * qb + 63, ntc = ((((tmax - 31) >> 4) + 1) + 63) >> 6;
;     const int ncv = (t >= 31) ? ((t - 31) >> 4) + 1 : 0;
;     const bf16* kcb = (const bf16*)(a.ws + WS_KCB) + (size_t)((b * 2 + kvh) * 256) * 128; const bf16* vct = (const bf16*)(a.ws + WS_VCT) + (size_t)((b * 2 + kvh) * 128) * 256;
;     __syncthreads();
; #pragma unroll
;     for (int ct = 0; ct < 4; ++ct) if (ct < ntc) { u32x4 k0, k1; nsa_ld2(kcb + (size_t)ct * 64 * 128, offkc, k0, k1); nsa_st_k(lds + ct * NBUF, tid, k0, k1); }
;     __syncthreads();
;     float mx = -1e30f, ls = 0.f;
; #pragma unroll 1
;     for (int ct = 0; ct < ntc; ++ct) { f32x16 s0, s1; nsa_qk(lds + ct * NBUF, qf, r, h, s0, s1);
.LBB0_1720:
	s_and_b64 s[0:1], s[2:3], exec
	v_readfirstlane_b32 s61, v0
	s_cselect_b32 s62, s78, s77
	s_lshr_b32 s68, s61, 6
	s_lshl_b32 s63, s68, 3
	v_or_b32_e32 v249, s63, v236
	v_lshl_add_u32 v233, s62, 6, v249
	v_add_u32_e32 v253, s79, v233
	v_mul_lo_u32 v34, v253, s73
	v_add_u32_e32 v35, v246, v34
	global_load_dwordx4 v[126:129], v35, s[28:29]
	global_load_dwordx4 v[130:133], v35, s[28:29] offset:32
	global_load_dwordx4 v[158:161], v35, s[28:29] offset:64
	global_load_dwordx4 v[162:165], v35, s[28:29] offset:96
	global_load_dwordx4 v[166:169], v35, s[28:29] offset:128
	global_load_dwordx4 v[170:173], v35, s[28:29] offset:160
	global_load_dwordx4 v[174:177], v35, s[28:29] offset:192
	global_load_dwordx4 v[178:181], v35, s[28:29] offset:224
	v_add_u32_e32 v34, v247, v34
	global_load_dword v80, v34, s[28:29]
	global_load_ushort v46, v34, s[28:29] offset:4
	s_lshl_b32 s0, s62, 2
	s_addk_i32 s0, 0x42
	s_ashr_i32 s22, s0, 6
	s_cmp_gt_i32 s22, 0
	s_cselect_b64 s[56:57], -1, 0
	s_cmp_lt_i32 s22, 1
	s_cselect_b64 s[14:15], -1, 0
	s_and_b64 vcc, exec, s[56:57]
	s_barrier
	s_cmp_gt_i32 s22, 1
	s_cselect_b64 s[0:1], -1, 0
	s_cmp_gt_i32 s22, 2
	s_cselect_b64 s[16:17], -1, 0
	s_cmp_gt_i32 s22, 3
	s_cselect_b64 s[18:19], -1, 0
	s_cmp_lt_i32 s22, 1
	s_cbranch_scc1 .Lkc_wait_1
	v_lshl_add_u64 v[34:35], s[36:37], 0, v[240:241]
	global_load_dwordx4 v[48:51], v[34:35], off
	global_load_dwordx4 v[52:55], v[34:35], off offset:16
	s_cmp_lt_i32 s22, 2
	s_cbranch_scc1 .Lkc_wait_1
	v_lshl_add_u64 v[34:35], s[40:41], 0, v[240:241]
	global_load_dwordx4 v[56:59], v[34:35], off
	global_load_dwordx4 v[60:63], v[34:35], off offset:16
	s_cmp_lt_i32 s22, 3
	s_cbranch_scc1 .Lkc_wait_1
	v_lshl_add_u64 v[34:35], s[42:43], 0, v[240:241]
	global_load_dwordx4 v[64:67], v[34:35], off
	global_load_dwordx4 v[68:71], v[34:35], off offset:16
	s_cmp_lt_i32 s22, 4
	s_cbranch_scc1 .Lkc_wait_1
	v_lshl_add_u64 v[34:35], s[44:45], 0, v[240:241]
	global_load_dwordx4 v[72:75], v[34:35], off
	global_load_dwordx4 v[76:79], v[34:35], off offset:16
.Lkc_wait_1:
	s_waitcnt vmcnt(0)
	s_cmp_lt_i32 s22, 1
	s_cbranch_scc1 .Lkc_done_1
	ds_write_b128 v242, v[48:51]
	ds_write_b128 v242, v[52:55] offset:16
	s_cmp_lt_i32 s22, 2
	s_cbranch_scc1 .Lkc_done_1
	ds_write_b128 v242, v[56:59] offset:17408
	ds_write_b128 v242, v[60:63] offset:17424
	s_cmp_lt_i32 s22, 3
	s_cbranch_scc1 .Lkc_done_1
	ds_write_b128 v242, v[64:67] offset:34816
	ds_write_b128 v242, v[68:71] offset:34832
	s_cmp_lt_i32 s22, 4
	s_cbranch_scc1 .Lkc_done_1
	ds_write_b128 v242, v[72:75] offset:52224
	ds_write_b128 v242, v[76:79] offset:52240
.Lkc_done_1:
.LBB0_1726:
	v_cmp_lt_i32_e64 s[12:13], 30, v233
	s_mov_b64 s[20:21], -1
	s_andn2_b64 vcc, exec, s[14:15]
	v_mbcnt_hi_u32_b32 v84, -1, v243
	s_waitcnt lgkmcnt(0)
	s_barrier
	s_cbranch_vccnz .LBB0_1728
	v_mbcnt_hi_u32_b32 v85, -1, v243
	v_and_b32_e32 v34, 64, v85
	v_xor_b32_e32 v83, 32, v85
	v_add_u32_e32 v43, 64, v34
	s_mov_b64 s[20:21], 0

; #define LAS __attribute__((address_space(3)))
; __device__ __forceinline__ void nsa_qk(const LAS unsigned char* kbuf, const bf16x8 (&qf)[8], int r, int h, f32x16& p0, f32x16& p1) {
;     const LAS unsigned char* kp = kbuf + r * NK_ROW + h * 16;
; #pragma unroll
;     for (int i = 0; i < 16; ++i) { p0[i] = 0.f; p1[i] = 0.f; }
;     bf16x8 a0[NSA_QKB], a1[NSA_QKB], b0[NSA_QKB], b1[NSA_QKB];
; #pragma unroll
;     for (int k4 = 0; k4 < NSA_QKB; ++k4) { a0[k4] = *(const LAS bf16x8*)(kp + k4 * 32); a1[k4] = *(const LAS bf16x8*)(kp + 32 * NK_ROW + k4 * 32); }
;     __builtin_amdgcn_sched_barrier(0);
; #pragma unroll
;     for (int kb = 0; kb < 8 / NSA_QKB; kb += 2) {
;         if (kb + 1 < 8 / NSA_QKB) {
; #pragma unroll
;             for (int k4 = 0; k4 < NSA_QKB; ++k4) { b0[k4] = *(const LAS bf16x8*)(kp + (NSA_QKB * (kb + 1) + k4) * 32); b1[k4] = *(const LAS bf16x8*)(kp + 32 * NK_ROW + (NSA_QKB * (kb + 1) + k4) * 32); } }
;         __builtin_amdgcn_sched_barrier(0);
; #pragma unroll
;         for (int k4 = 0; k4 < NSA_QKB; ++k4) { p0 = __builtin_amdgcn_mfma_f32_32x32x16_bf16(a0[k4], qf[NSA_QKB * kb + k4], p0, 0, 0, 0); p1 = __builtin_amdgcn_mfma_f32_32x32x16_bf16(a1[k4], qf[NSA_QKB * kb + k4], p1, 0, 0, 0); }
;         __builtin_amdgcn_sched_barrier(0);
;         if (kb + 2 < 8 / NSA_QKB) {
; #pragma unroll
;             for (int k4 = 0; k4 < NSA_QKB; ++k4) { a0[k4] = *(const LAS bf16x8*)(kp + (NSA_QKB * (kb + 2) + k4) * 32); a1[k4] = *(const LAS bf16x8*)(kp + 32 * NK_ROW + (NSA_QKB * (kb + 2) + k4) * 32); } }
;         __builtin_amdgcn_sched_barrier(0);
;         if (kb + 1 < 8 / NSA_QKB) {
; #pragma unroll
;             for (int k4 = 0; k4 < NSA_QKB; ++k4) { p0 = __builtin_amdgcn_mfma_f32_32x32x16_bf16(b0[k4], qf[NSA_QKB * (kb + 1) + k4], p0, 0, 0, 0); p1 = __builtin_amdgcn_mfma_f32_32x32x16_bf16(b1[k4], qf[NSA_QKB * (kb + 1) + k4], p1, 0, 0, 0); } }
;         __builtin_amdgcn_sched_barrier(0);
;     }
; }
; __device__ __forceinline__ void nsa_unit(const Args& a, LAS unsigned char* lds, int b, int kvh, int qb) {
;     ...
; #pragma unroll 1
;     for (int ct = 0; ct < ntc; ++ct) { f32x16 s0, s1; nsa_qk(lds + ct * NBUF, qf, r, h, s0, s1);
; #pragma unroll
;         for (int i = 0; i < 16; ++i) { const int c0 = 64 * ct + (i & 3) + 8 * (i >> 2) + 4 * h; s0[i] = (c0 < ncv) ? s0[i] : NINF; s1[i] = (c0 + 32 < ncv) ? s1[i] : NINF; }
.LBB0_1730:
	v_mov_b32_e32 v89, v48
	ds_read_b128 v[48:51], v86 offset:8704
	ds_read_b128 v[52:55], v86
	ds_read_b128 v[90:93], v86 offset:32
	ds_read_b128 v[94:97], v86 offset:8736
	ds_read_b128 v[98:101], v86 offset:64
	ds_read_b128 v[102:105], v86 offset:96
	ds_read_b128 v[106:109], v86 offset:8768
	ds_read_b128 v[110:113], v86 offset:8800
	s_waitcnt vmcnt(9) lgkmcnt(6)
	v_mfma_f32_32x32x16_bf16 v[64:79], v[52:55], v[126:129], 0
	v_mfma_f32_32x32x16_bf16 v[48:63], v[48:51], v[126:129], 0
	s_waitcnt vmcnt(8) lgkmcnt(4)
	v_mfma_f32_32x32x16_bf16 v[48:63], v[94:97], v[130:133], v[48:63]
	v_mfma_f32_32x32x16_bf16 v[64:79], v[90:93], v[130:133], v[64:79]
	ds_read_b128 v[90:93], v86 offset:8864
	ds_read_b128 v[94:97], v86 offset:8832
	ds_read_b128 v[114:117], v86 offset:128
	ds_read_b128 v[118:121], v86 offset:160
	s_waitcnt vmcnt(7) lgkmcnt(5)
	v_mfma_f32_32x32x16_bf16 v[48:63], v[106:109], v[158:161], v[48:63]
	v_mfma_f32_32x32x16_bf16 v[64:79], v[98:101], v[158:161], v[64:79]
	s_waitcnt vmcnt(6) lgkmcnt(4)
	v_mfma_f32_32x32x16_bf16 v[48:63], v[110:113], v[162:165], v[48:63]
	v_mfma_f32_32x32x16_bf16 v[64:79], v[102:105], v[162:165], v[64:79]
	ds_read_b128 v[98:101], v86 offset:192
	ds_read_b128 v[102:105], v86 offset:224
	ds_read_b128 v[106:109], v86 offset:8896
	ds_read_b128 v[110:113], v86 offset:8928
	s_waitcnt vmcnt(5) lgkmcnt(6)
	v_mfma_f32_32x32x16_bf16 v[48:63], v[94:97], v[166:169], v[48:63]
	s_waitcnt lgkmcnt(5)
	v_mfma_f32_32x32x16_bf16 v[64:79], v[114:117], v[166:169], v[64:79]
	s_waitcnt vmcnt(4)
	v_mfma_f32_32x32x16_bf16 v[48:63], v[90:93], v[170:173], v[48:63]
	s_waitcnt lgkmcnt(4)
	v_mfma_f32_32x32x16_bf16 v[64:79], v[118:121], v[170:173], v[64:79]
	s_waitcnt vmcnt(3) lgkmcnt(1)
	v_mfma_f32_32x32x16_bf16 v[48:63], v[106:109], v[174:177], v[48:63]
	v_mfma_f32_32x32x16_bf16 v[64:79], v[98:101], v[174:177], v[64:79]
	s_waitcnt vmcnt(2) lgkmcnt(0)
	v_mfma_f32_32x32x16_bf16 v[48:63], v[110:113], v[178:181], v[48:63]
	v_mfma_f32_32x32x16_bf16 v[64:79], v[102:105], v[178:181], v[64:79]
	v_subrev_u32_e32 v34, 59, v87
	v_cmp_lt_u32_e32 vcc, v34, v81
	v_subrev_u32_e32 v35, 27, v87
	v_subrev_u32_e32 v36, 58, v87
	s_nop 7
	v_cndmask_b32_e32 v34, v244, v64, vcc
	v_cmp_lt_u32_e32 vcc, v35, v81
	v_subrev_u32_e32 v37, 26, v87
	v_subrev_u32_e32 v38, 57, v87
	v_cndmask_b32_e32 v35, v244, v48, vcc
	v_cmp_lt_u32_e32 vcc, v36, v81
	v_subrev_u32_e32 v39, 25, v87
	v_subrev_u32_e32 v40, 56, v87
	v_cndmask_b32_e32 v36, v244, v65, vcc
	v_cmp_lt_u32_e32 vcc, v37, v81
	v_subrev_u32_e32 v41, 24, v87
	v_subrev_u32_e32 v48, 51, v87
	v_cndmask_b32_e32 v37, v244, v49, vcc
	v_cmp_lt_u32_e32 vcc, v38, v81
	v_subrev_u32_e32 v49, 19, v87
	s_add_i32 s22, s22, -1
	v_cndmask_b32_e32 v38, v244, v66, vcc
	v_cmp_lt_u32_e32 vcc, v39, v81
	v_add_u32_e32 v86, 0x4400, v86
	s_cmp_eq_u32 s22, 0
	v_cndmask_b32_e32 v39, v244, v50, vcc
	v_cmp_lt_u32_e32 vcc, v40, v81
	s_nop 1
	v_cndmask_b32_e32 v40, v244, v67, vcc
	v_cmp_lt_u32_e32 vcc, v41, v81
	s_nop 1
	v_cndmask_b32_e32 v41, v244, v51, vcc
	v_cmp_lt_u32_e32 vcc, v48, v81
	s_nop 1
	v_cndmask_b32_e32 v48, v244, v68, vcc
	v_cmp_lt_u32_e32 vcc, v49, v81
	v_subrev_u32_e32 v49, 50, v87
	s_nop 0
	v_cndmask_b32_e32 v50, v244, v52, vcc
	v_cmp_lt_u32_e32 vcc, v49, v81
	v_subrev_u32_e32 v49, 18, v87
	s_nop 0
	v_cndmask_b32_e32 v51, v244, v69, vcc
	v_cmp_lt_u32_e32 vcc, v49, v81
	v_subrev_u32_e32 v49, 49, v87
	s_nop 0
	v_cndmask_b32_e32 v52, v244, v53, vcc
	v_cmp_lt_u32_e32 vcc, v49, v81
	v_subrev_u32_e32 v49, 17, v87
	s_nop 0
	v_cndmask_b32_e32 v53, v244, v70, vcc
	v_cmp_lt_u32_e32 vcc, v49, v81
	v_subrev_u32_e32 v49, 48, v87
	s_nop 0
	v_cndmask_b32_e32 v54, v244, v54, vcc
	v_cmp_lt_u32_e32 vcc, v49, v81
	v_add_u32_e32 v49, -16, v87
	s_nop 0
	v_cndmask_b32_e32 v64, v244, v71, vcc
	v_cmp_lt_u32_e32 vcc, v49, v81
	v_subrev_u32_e32 v49, 43, v87
	s_nop 0
	v_cndmask_b32_e32 v55, v244, v55, vcc
	v_cmp_lt_u32_e32 vcc, v49, v81
	v_add_u32_e32 v49, -11, v87
	s_nop 0
	v_cndmask_b32_e32 v65, v244, v72, vcc
	v_cmp_lt_u32_e32 vcc, v49, v81
	v_subrev_u32_e32 v49, 42, v87
	s_nop 0
	v_cndmask_b32_e32 v56, v244, v56, vcc
	v_cmp_lt_u32_e32 vcc, v49, v81
	v_add_u32_e32 v49, -10, v87
	s_nop 0
	v_cndmask_b32_e32 v66, v244, v73, vcc
	v_cmp_lt_u32_e32 vcc, v49, v81
	v_subrev_u32_e32 v49, 41, v87
	v_max_f32_e32 v73, v36, v36
	v_cndmask_b32_e32 v57, v244, v57, vcc
	v_cmp_lt_u32_e32 vcc, v49, v81
	v_add_u32_e32 v49, -9, v87
	s_nop 0
	v_cndmask_b32_e32 v67, v244, v74, vcc
	v_cmp_lt_u32_e32 vcc, v49, v81
	v_subrev_u32_e32 v49, 40, v87
	v_max_f32_e32 v74, v38, v38
	v_cndmask_b32_e32 v58, v244, v58, vcc
	v_cmp_lt_u32_e32 vcc, v49, v81
	v_add_u32_e32 v49, -8, v87
	s_nop 0
	v_cndmask_b32_e32 v68, v244, v75, vcc
	v_cmp_lt_u32_e32 vcc, v49, v81
	v_subrev_u32_e32 v49, 35, v87
	v_max_f32_e32 v75, v40, v40
	v_cndmask_b32_e32 v59, v244, v59, vcc
	v_cmp_lt_u32_e32 vcc, v49, v81
	v_add_u32_e32 v49, -3, v87
	s_nop 0
	v_cndmask_b32_e32 v69, v244, v76, vcc
	v_cmp_lt_u32_e32 vcc, v49, v81
	v_subrev_u32_e32 v49, 34, v87
	s_nop 0
	v_cndmask_b32_e32 v60, v244, v60, vcc
	v_cmp_lt_u32_e32 vcc, v49, v81
	v_add_u32_e32 v49, -2, v87
	s_nop 0
	v_cndmask_b32_e32 v70, v244, v77, vcc
	v_cmp_lt_u32_e32 vcc, v49, v81
	v_subrev_u32_e32 v49, 33, v87
	s_nop 0
	v_cndmask_b32_e32 v61, v244, v61, vcc
; __device__ __forceinline__ void nsa_ld2(const bf16* base, unsigned off, u32x4& k0, u32x4& k1) { const gcp p = uniform_ptr(base) + off; k0 = gld<u32x4>(p); k1 = gld<u32x4>(p + 16); }
; __device__ __forceinline__ void nsa_unit(const Args& a, LAS unsigned char* lds, int b, int kvh, int qb) {
;     ...
;     for (int ct = 0; ct < 4; ++ct) if (ct < ntc) { u32x4 k0, k1; nsa_ld2(kcb + (size_t)ct * 64 * 128, offkc, k0, k1); nsa_st_k(lds + ct * NBUF, tid, k0, k1); }
;     ...
;         float tmx = nsa_rowmax(s0, s1); tmx = fmaxf(tmx, __shfl_xor(tmx, 32));
;         const float mnew = fmaxf(mx, tmx), alpha = __builtin_amdgcn_exp2f((mx - mnew) * SM_C), nmc = -mnew * SM_C; mx = mnew;
;         float la = 0.f;
; #pragma unroll
;         for (int i = 0; i < 16; ++i) la += __builtin_amdgcn_exp2f(fmaf(s0[i], SM_C, nmc)) + __builtin_amdgcn_exp2f(fmaf(s1[i], SM_C, nmc));
;         ls = ls * alpha + la; }
	v_cmp_lt_u32_e32 vcc, v49, v81
	v_add_u32_e32 v49, -1, v87
	s_nop 0
	v_cndmask_b32_e32 v71, v244, v78, vcc
	v_cmp_lt_u32_e32 vcc, v49, v81
	v_subrev_u32_e32 v49, 32, v87
	s_nop 0
	v_cndmask_b32_e32 v62, v244, v62, vcc
	v_cmp_lt_u32_e32 vcc, v49, v81
	v_max_f32_e32 v49, v37, v37
	v_max_f32_e32 v49, v73, v49
	v_max_f32_e32 v73, v39, v39
	v_max_f32_e32 v73, v74, v73
	v_max_f32_e32 v74, v41, v41
	v_max3_f32 v49, v34, v35, v49
	v_max_f32_e32 v74, v75, v74
	v_max3_f32 v49, v49, v73, v74
	v_max_f32_e32 v73, v50, v50
	v_max_f32_e32 v74, v48, v48
	v_max_f32_e32 v73, v74, v73
	v_max_f32_e32 v74, v52, v52
	v_max_f32_e32 v75, v51, v51
	v_max_f32_e32 v74, v75, v74
	v_max3_f32 v49, v49, v73, v74
	v_max_f32_e32 v73, v54, v54
	v_max_f32_e32 v74, v53, v53
	v_max_f32_e32 v73, v74, v73
	v_max_f32_e32 v74, v55, v55
	v_max_f32_e32 v75, v64, v64
	v_max_f32_e32 v74, v75, v74
	v_max3_f32 v49, v49, v73, v74
	v_max_f32_e32 v73, v56, v56
	v_max_f32_e32 v74, v65, v65
	v_max_f32_e32 v73, v74, v73
	v_max_f32_e32 v74, v57, v57
	v_max_f32_e32 v75, v66, v66
	v_max_f32_e32 v74, v75, v74
	v_max3_f32 v49, v49, v73, v74
	v_max_f32_e32 v73, v58, v58
	v_max_f32_e32 v74, v67, v67
	v_max_f32_e32 v73, v74, v73
	v_max_f32_e32 v74, v59, v59
	v_max_f32_e32 v75, v68, v68
	v_max_f32_e32 v74, v75, v74
	v_max3_f32 v49, v49, v73, v74
	v_max_f32_e32 v73, v60, v60
	v_max_f32_e32 v74, v69, v69
	v_max_f32_e32 v73, v74, v73
	v_max_f32_e32 v74, v61, v61
	v_max_f32_e32 v75, v70, v70
	v_cndmask_b32_e32 v72, v244, v79, vcc
	v_cmp_lt_u32_e32 vcc, v87, v81
	v_max_f32_e32 v74, v75, v74
	v_max3_f32 v49, v49, v73, v74
	v_cndmask_b32_e32 v63, v244, v63, vcc
	v_max_f32_e32 v73, v62, v62
	v_max_f32_e32 v74, v71, v71
	v_max_f32_e32 v73, v74, v73
	v_max_f32_e32 v74, v63, v63
	v_max_f32_e32 v75, v72, v72
	v_max_f32_e32 v74, v75, v74
	v_max3_f32 v49, v49, v73, v74
	ds_bpermute_b32 v73, v85, v49
	v_add_u32_e32 v87, 64, v87
	s_waitcnt lgkmcnt(0)
	v_max3_f32 v49, v88, v49, v73
	v_mul_f32_e32 v82, 0xbe0293ee, v49
	v_fmamk_f32 v34, v34, 0x3e0293ee, v82
	v_fmamk_f32 v35, v35, 0x3e0293ee, v82
	v_exp_f32_e32 v34, v34
	v_exp_f32_e32 v35, v35
	v_sub_f32_e32 v73, v88, v49
	v_mul_f32_e32 v73, 0x3e0293ee, v73
	v_mov_b32_e32 v88, v49
	v_add_f32_e32 v34, v34, v35
	v_fmamk_f32 v35, v36, 0x3e0293ee, v82
	v_fmamk_f32 v36, v37, 0x3e0293ee, v82
	v_exp_f32_e32 v35, v35
	v_exp_f32_e32 v36, v36
	v_add_f32_e32 v34, 0, v34
	v_add_f32_e32 v35, v35, v36
	v_add_f32_e32 v34, v35, v34
	v_fmamk_f32 v35, v38, 0x3e0293ee, v82
	v_fmamk_f32 v36, v39, 0x3e0293ee, v82
	v_exp_f32_e32 v35, v35
	v_exp_f32_e32 v36, v36
	s_nop 0
	v_add_f32_e32 v35, v35, v36
	v_add_f32_e32 v34, v35, v34
	v_fmamk_f32 v35, v40, 0x3e0293ee, v82
	v_fmamk_f32 v36, v41, 0x3e0293ee, v82
	v_exp_f32_e32 v35, v35
	v_exp_f32_e32 v36, v36
	s_nop 0
	v_add_f32_e32 v35, v35, v36
	v_add_f32_e32 v38, v35, v34
	v_fmamk_f32 v34, v48, 0x3e0293ee, v82
	v_exp_f32_e32 v35, v34
	v_fmamk_f32 v34, v50, 0x3e0293ee, v82
	v_exp_f32_e32 v37, v34
	v_fmamk_f32 v34, v51, 0x3e0293ee, v82
	v_fmamk_f32 v36, v52, 0x3e0293ee, v82
	v_exp_f32_e32 v34, v34
	v_exp_f32_e32 v36, v36
	s_nop 0
	v_pk_add_f32 v[34:35], v[34:35], v[36:37]
	s_nop 0
	v_add_f32_e32 v35, v35, v38
	v_add_f32_e32 v38, v34, v35
	v_fmamk_f32 v34, v53, 0x3e0293ee, v82
	v_exp_f32_e32 v35, v34
	v_fmamk_f32 v34, v54, 0x3e0293ee, v82
	v_exp_f32_e32 v37, v34
	v_fmamk_f32 v34, v64, 0x3e0293ee, v82
	v_fmamk_f32 v36, v55, 0x3e0293ee, v82
	v_exp_f32_e32 v34, v34
	v_exp_f32_e32 v36, v36
	s_nop 0
	v_pk_add_f32 v[34:35], v[34:35], v[36:37]
	s_nop 0
	v_add_f32_e32 v35, v35, v38
	v_add_f32_e32 v38, v34, v35
	v_fmamk_f32 v34, v65, 0x3e0293ee, v82
	v_exp_f32_e32 v35, v34
	v_fmamk_f32 v34, v56, 0x3e0293ee, v82
	v_exp_f32_e32 v37, v34
	v_fmamk_f32 v34, v66, 0x3e0293ee, v82
	v_fmamk_f32 v36, v57, 0x3e0293ee, v82
	v_exp_f32_e32 v34, v34
	v_exp_f32_e32 v36, v36
	s_nop 0
	v_pk_add_f32 v[34:35], v[34:35], v[36:37]
	s_nop 0
	v_add_f32_e32 v35, v35, v38
	v_add_f32_e32 v38, v34, v35
	v_fmamk_f32 v34, v67, 0x3e0293ee, v82
	v_exp_f32_e32 v35, v34
	v_fmamk_f32 v34, v58, 0x3e0293ee, v82
	v_exp_f32_e32 v37, v34
	v_fmamk_f32 v34, v68, 0x3e0293ee, v82
	v_fmamk_f32 v36, v59, 0x3e0293ee, v82
	v_exp_f32_e32 v34, v34
	v_exp_f32_e32 v36, v36
	s_nop 0
	v_pk_add_f32 v[34:35], v[34:35], v[36:37]
	s_nop 0
	v_add_f32_e32 v35, v35, v38
	v_add_f32_e32 v38, v34, v35
	v_fmamk_f32 v34, v69, 0x3e0293ee, v82
	v_exp_f32_e32 v35, v34
	v_fmamk_f32 v34, v60, 0x3e0293ee, v82
	v_exp_f32_e32 v37, v34
	v_fmamk_f32 v34, v70, 0x3e0293ee, v82
	v_fmamk_f32 v36, v61, 0x3e0293ee, v82
	v_exp_f32_e32 v34, v34
	v_exp_f32_e32 v36, v36
	s_nop 0
	v_pk_add_f32 v[34:35], v[34:35], v[36:37]
	s_nop 0
	v_add_f32_e32 v35, v35, v38
	v_add_f32_e32 v38, v34, v35
	v_fmamk_f32 v34, v71, 0x3e0293ee, v82
	v_exp_f32_e32 v35, v34
	v_fmamk_f32 v34, v62, 0x3e0293ee, v82
	v_exp_f32_e32 v37, v34
	v_fmamk_f32 v34, v72, 0x3e0293ee, v82
	v_fmamk_f32 v36, v63, 0x3e0293ee, v82
	v_exp_f32_e32 v34, v34
	v_exp_f32_e32 v36, v36
	s_nop 0
	v_pk_add_f32 v[34:35], v[34:35], v[36:37]
	s_nop 0
	v_add_f32_e32 v35, v35, v38
	v_add_f32_e32 v48, v34, v35
	v_exp_f32_e32 v34, v73
	s_nop 0
	v_fmac_f32_e32 v48, v89, v34
	s_cbranch_scc0 .LBB0_1730
	v_mov_b32_e32 v85, v84
	s_branch .LBB0_1735
.LBB0_1734:
	v_mov_b32_e32 v82, 0x6fce03f9
	v_mov_b32_e32 v48, 0

; __device__ __forceinline__ void nsa_unit(const Args& a, LAS unsigned char* lds, int b, int kvh, int qb) {
;     ...
;     for (int qq = 0; qq < 8; ++qq) {
;         const float imp = impw[qq * 64 + lane] + (lane > 0 ? impw[512 + qq * 64 + lane - 1] : 0.f);
;         const float iv = (lane > qb) ? NINF : ((lane == 0 || lane == qb || lane == qb - 1) ? 1e9f : imp);
;         const unsigned ub = __builtin_bit_cast(unsigned, iv); unsigned key = (ub & 0x80000000u) ? ~ub : (ub | 0x80000000u); key = (key & ~63u) | (unsigned)(63 - lane);
;         unsigned thr = 0u;
; #pragma unroll
;     ...
;         const unsigned long long msk = __ballot(key >= thr);
;         if (lane == 0) { selw[qq * 2] = (unsigned)msk; selw[qq * 2 + 1] = (unsigned)(msk >> 32); }
;     }
.LBB0_1815:
	v_add_u32_e32 v34, 0xfffff804, v43
	ds_read_b32 v46, v34
	v_mov_b32_e32 v80, 0
	s_and_saveexec_b64 s[0:1], s[10:11]
	ds_read_b32 v80, v43
	s_or_b64 exec, exec, s[0:1]
	s_waitcnt lgkmcnt(0)
	v_add_f32_e32 v34, v46, v80
	v_mov_b32_e32 v35, 0x4e6e6b28
	v_cndmask_b32_e64 v34, v34, v35, s[20:21]
	v_cndmask_b32_e32 v34, v34, v244, vcc
	v_not_b32_e32 v35, v34
	v_cmp_gt_i32_e64 s[22:23], 0, v34
	s_nop 1
	v_cndmask_b32_e64 v34, -|v34|, v35, s[22:23]
	v_cmp_gt_i32_e64 s[22:23], 0, v34
	s_bcnt1_i32_b64 s24, s[22:23]
	s_cmp_gt_u32 s24, 15
	v_and_b32_e32 v35, 0xffffffc0, v34
	s_cselect_b32 s2, 0x80000000, 0
	v_bitop3_b32 v35, v35, 63, v223 bitop3:0x36
	s_or_b32 s3, s2, 2.0
	v_cmp_le_u32_e64 s[22:23], s3, v35
	s_bcnt1_i32_b64 s24, s[22:23]
	s_cmp_gt_u32 s24, 15
	s_cselect_b32 s2, s3, s2
	s_or_b32 s3, s2, 0x20000000
	v_cmp_le_u32_e64 s[22:23], s3, v35
	s_bcnt1_i32_b64 s24, s[22:23]
	s_cmp_gt_u32 s24, 15
	s_cselect_b32 s2, s3, s2
	s_or_b32 s3, s2, 0x10000000
	v_cmp_le_u32_e64 s[22:23], s3, v35
	s_bcnt1_i32_b64 s24, s[22:23]
	s_cmp_gt_u32 s24, 15
	s_cselect_b32 s2, s3, s2
	s_or_b32 s3, s2, 0x8000000
	v_cmp_le_u32_e64 s[22:23], s3, v35
	s_bcnt1_i32_b64 s24, s[22:23]
	s_cmp_gt_u32 s24, 15
	s_cselect_b32 s2, s3, s2
	s_or_b32 s3, s2, 0x4000000
	v_cmp_le_u32_e64 s[22:23], s3, v35
	s_bcnt1_i32_b64 s24, s[22:23]
	s_cmp_gt_u32 s24, 15
	s_cselect_b32 s2, s3, s2
	s_or_b32 s3, s2, 0x2000000
	v_cmp_le_u32_e64 s[22:23], s3, v35
	s_bcnt1_i32_b64 s24, s[22:23]
	s_cmp_gt_u32 s24, 15
	s_cselect_b32 s2, s3, s2
	s_or_b32 s3, s2, 0x1000000
	v_cmp_le_u32_e64 s[22:23], s3, v35
	s_bcnt1_i32_b64 s24, s[22:23]
	s_cmp_gt_u32 s24, 15
	s_cselect_b32 s2, s3, s2
	s_or_b32 s3, s2, 0x800000
	v_cmp_le_u32_e64 s[22:23], s3, v35
	s_bcnt1_i32_b64 s24, s[22:23]
	s_cmp_gt_u32 s24, 15
	s_cselect_b32 s2, s3, s2
	s_or_b32 s3, s2, 0x400000
	v_cmp_le_u32_e64 s[22:23], s3, v35
	s_bcnt1_i32_b64 s24, s[22:23]
	s_cmp_gt_u32 s24, 15
	s_cselect_b32 s2, s3, s2
	s_or_b32 s3, s2, 0x200000
	v_cmp_le_u32_e64 s[22:23], s3, v35
	s_bcnt1_i32_b64 s24, s[22:23]
	s_cmp_gt_u32 s24, 15
	s_cselect_b32 s2, s3, s2
	s_or_b32 s3, s2, 0x100000
	v_cmp_le_u32_e64 s[22:23], s3, v35
	s_bcnt1_i32_b64 s24, s[22:23]
	s_cmp_gt_u32 s24, 15
	s_cselect_b32 s2, s3, s2
	s_or_b32 s3, s2, 0x80000
	v_cmp_le_u32_e64 s[22:23], s3, v35
	s_bcnt1_i32_b64 s24, s[22:23]
	s_cmp_gt_u32 s24, 15
	s_cselect_b32 s2, s3, s2
	s_or_b32 s3, s2, 0x40000
	v_cmp_le_u32_e64 s[22:23], s3, v35
	s_bcnt1_i32_b64 s24, s[22:23]
	s_cmp_gt_u32 s24, 15
	s_cselect_b32 s2, s3, s2
	s_or_b32 s3, s2, 0x20000
	v_cmp_le_u32_e64 s[22:23], s3, v35
	s_bcnt1_i32_b64 s24, s[22:23]
	s_cmp_gt_u32 s24, 15
	s_cselect_b32 s2, s3, s2
	s_or_b32 s3, s2, 0x10000
	v_cmp_le_u32_e64 s[22:23], s3, v35
	s_bcnt1_i32_b64 s24, s[22:23]
	s_cmp_gt_u32 s24, 15
	s_cselect_b32 s2, s3, s2
	s_or_b32 s3, s2, 0x8000
	v_cmp_le_u32_e64 s[22:23], s3, v35
	s_bcnt1_i32_b64 s24, s[22:23]
	s_cmp_gt_u32 s24, 15
	s_cselect_b32 s2, s3, s2
	s_or_b32 s3, s2, 0x4000
	v_cmp_le_u32_e64 s[22:23], s3, v35
	s_bcnt1_i32_b64 s24, s[22:23]
	s_cmp_gt_u32 s24, 15
	s_cselect_b32 s2, s3, s2
	s_or_b32 s3, s2, 0x2000
	v_cmp_le_u32_e64 s[22:23], s3, v35
	s_bcnt1_i32_b64 s24, s[22:23]
	s_cmp_gt_u32 s24, 15
	s_cselect_b32 s2, s3, s2
	s_or_b32 s3, s2, 0x1000
	v_cmp_le_u32_e64 s[22:23], s3, v35
	s_bcnt1_i32_b64 s24, s[22:23]
	s_cmp_gt_u32 s24, 15
	s_cselect_b32 s2, s3, s2
	s_or_b32 s3, s2, 0x800
	v_cmp_le_u32_e64 s[22:23], s3, v35
	s_bcnt1_i32_b64 s24, s[22:23]
	s_cmp_gt_u32 s24, 15
	s_cselect_b32 s2, s3, s2
	s_or_b32 s3, s2, 0x400
	v_cmp_le_u32_e64 s[22:23], s3, v35
	s_bcnt1_i32_b64 s24, s[22:23]
	s_cmp_gt_u32 s24, 15
	s_cselect_b32 s2, s3, s2
	s_or_b32 s3, s2, 0x200
	v_cmp_le_u32_e64 s[22:23], s3, v35
	s_bcnt1_i32_b64 s24, s[22:23]
	s_cmp_gt_u32 s24, 15
	s_cselect_b32 s2, s3, s2
	s_or_b32 s3, s2, 0x100
	v_cmp_le_u32_e64 s[22:23], s3, v35
	s_bcnt1_i32_b64 s24, s[22:23]
	s_cmp_gt_u32 s24, 15
	s_cselect_b32 s2, s3, s2
	s_or_b32 s3, s2, 0x80
	v_cmp_le_u32_e64 s[22:23], s3, v35
	s_bcnt1_i32_b64 s24, s[22:23]
	s_cmp_gt_u32 s24, 15
	s_cselect_b32 s2, s3, s2
	s_or_b32 s3, s2, 64
	v_cmp_le_u32_e64 s[22:23], s3, v35
	s_bcnt1_i32_b64 s24, s[22:23]
	s_cmp_gt_u32 s24, 15
	s_cselect_b32 s2, s3, s2
	s_or_b32 s3, s2, 32
	v_cmp_le_u32_e64 s[22:23], s3, v35
	s_bcnt1_i32_b64 s24, s[22:23]
	s_cmp_gt_u32 s24, 15
	s_cselect_b32 s2, s3, s2
	s_or_b32 s3, s2, 16
	v_cmp_le_u32_e64 s[22:23], s3, v35
	s_bcnt1_i32_b64 s24, s[22:23]
	s_cmp_gt_u32 s24, 15
	s_cselect_b32 s2, s3, s2
	s_or_b32 s3, s2, 8
	v_cmp_le_u32_e64 s[22:23], s3, v35
	s_bcnt1_i32_b64 s24, s[22:23]
	s_cmp_gt_u32 s24, 15
	s_cselect_b32 s2, s3, s2
	s_or_b32 s3, s2, 4
	v_cmp_le_u32_e64 s[22:23], s3, v35
	s_bcnt1_i32_b64 s24, s[22:23]
	s_cmp_gt_u32 s24, 15
	s_cselect_b32 s2, s3, s2
	s_or_b32 s3, s2, 2
	v_cmp_le_u32_e64 s[22:23], s3, v35
	s_bcnt1_i32_b64 s24, s[22:23]
	s_cmp_gt_u32 s24, 15
	s_cselect_b32 s2, s3, s2
	s_or_b32 s3, s2, 1
	v_cmp_le_u32_e64 s[22:23], s3, v35
	s_bcnt1_i32_b64 s24, s[22:23]
	s_cmp_gt_u32 s24, 15
	s_cselect_b32 s0, s3, s2
	v_cmp_le_u32_e64 s[2:3], s0, v35
	s_and_saveexec_b64 s[0:1], s[8:9]
	s_cbranch_execz .LBB0_1814
	s_add_i32 s22, s69, s70
	v_mov_b32_e32 v34, s22
	v_mov_b64_e32 v[36:37], s[2:3]
	ds_write_b64 v34, v[36:37]
	s_branch .LBB0_1814

; #define GAS __attribute__((address_space(1)))
; __device__ __forceinline__ unsigned cvt_pk_bf16(float lo, float hi) { unsigned r; asm volatile("v_cvt_pk_bf16_f32 %0, %1, %2" : "=v"(r) : "v"(lo), "v"(hi)); return r; }
; __device__ __forceinline__ gcp uniform_ptr(const void* p) { const unsigned long long v = (unsigned long long)p; const unsigned lo = __builtin_amdgcn_readfirstlane((unsigned)v), hi = __builtin_amdgcn_readfirstlane((unsigned)(v >> 32)); return (gcp)(((unsigned long long)hi << 32) | lo); }
; __device__ __forceinline__ void nsa_unit(const Args& a, LAS unsigned char* lds, int b, int kvh, int qb) {
;     ...
;     GAS unsigned char* mp = (GAS unsigned char*)uniform_ptr(a.ws + WS_MIX) + ((unsigned)m * 4096u + (unsigned)(((kvh * 4 + g) * 128 + 4 * h) * 2));
; #pragma unroll
;     for (int dt = 0; dt < 4; ++dt)
; #pragma unroll
;         for (int aa = 0; aa < 4; ++aa) { u32x2 wv; wv.x = pg8::cvt_pk_bf16(o[dt][4 * aa] * g0, o[dt][4 * aa + 1] * g0); wv.y = pg8::cvt_pk_bf16(o[dt][4 * aa + 2] * g0, o[dt][4 * aa + 3] * g0); *(GAS u32x2*)(mp + (32 * dt + 8 * aa) * 2) = wv; }
;     { const gcp rpb = uniform_ptr(a.ws + WS_ROPE) + (unsigned)((t * 32 + 8 * h) * 4);
;       u32x4 w0 = __builtin_bit_cast(u32x4, qf[0]), w1 = __builtin_bit_cast(u32x4, qf[1]);
; #pragma unroll
;       for (int jj = 0; jj < 4; ++jj) { const float c0 = gld<float>(rpb + 8 * jj), c1 = gld<float>(rpb + 8 * jj + 4), s0 = gld<float>(rpb + 64 + 8 * jj), s1 = gld<float>(rpb + 64 + 8 * jj + 4);
;           const float xa0 = bflo(w0[jj]), xa1 = bfhi(w0[jj]), xb0 = bflo(w1[jj]), xb1 = bfhi(w1[jj]);
;           w0[jj] = pg8::cvt_pk_bf16(xa0 * c0 - xb0 * s0, xa1 * c1 - xb1 * s1); w1[jj] = pg8::cvt_pk_bf16(xb0 * c0 + xa0 * s0, xb1 * c1 + xa1 * s1); }
;       qf[0] = __builtin_bit_cast(bf16x8, w0); qf[1] = __builtin_bit_cast(bf16x8, w1); }
;     const int nS = qb + 1, jlo = qb > 8 ? qb - 8 : 0, nTot = nS + (qb - jlo + 1);
;     const bf16* ksb = proj + (size_t)b * T * PW + PKS + kvh * 128; const bf16* kwb = proj + (size_t)b * T * PW + PKW + kvh * 128;
;     const bf16* vsb = (const bf16*)(a.ws + WS_VTS) + (size_t)((b * 2 + kvh) * 128) * VTP; const bf16* vwb = (const bf16*)(a.ws + WS_VTW) + (size_t)((b * 2 + kvh) * 128) * VTP;
.LBB0_1836:
	v_add_f32_e32 v34, 1.0, v254
	v_div_scale_f32 v35, s[0:1], v34, v34, 1.0
	v_rcp_f32_e32 v36, v35
	v_lshl_or_b32 v48, v253, 12, v248
	s_add_i32 s16, s62, 1
	s_not_b32 s2, s62
	v_fma_f32 v37, -v35, v36, 1.0
	v_fmac_f32_e32 v36, v37, v36
	v_div_scale_f32 v37, vcc, 1.0, v34, 1.0
	v_mul_f32_e32 v38, v37, v36
	v_fma_f32 v39, -v35, v38, v37
	v_fmac_f32_e32 v38, v39, v36
	v_fma_f32 v35, -v35, v38, v37
	v_div_fmas_f32 v35, v35, v36, v38
	v_div_fixup_f32 v36, v35, v34, 1.0
	v_mul_f32_e32 v34, v36, v110
	v_mul_f32_e32 v35, v36, v111
	v_cvt_pk_bf16_f32 v34, v34, v35
	v_mul_f32_e32 v35, v36, v112
	v_mul_f32_e32 v37, v36, v113
	v_cvt_pk_bf16_f32 v35, v35, v37
	global_store_dwordx2 v48, v[34:35], s[30:31]
	v_mul_f32_e32 v34, v36, v114
	v_mul_f32_e32 v35, v36, v115
	v_cvt_pk_bf16_f32 v34, v34, v35
	v_mul_f32_e32 v35, v36, v116
	v_mul_f32_e32 v37, v36, v117
	v_cvt_pk_bf16_f32 v35, v35, v37
	global_store_dwordx2 v48, v[34:35], s[30:31] offset:16
	v_mul_f32_e32 v34, v36, v118
	v_mul_f32_e32 v35, v36, v119
	v_cvt_pk_bf16_f32 v34, v34, v35
	v_mul_f32_e32 v35, v36, v120
	v_mul_f32_e32 v37, v36, v121
	v_cvt_pk_bf16_f32 v35, v35, v37
	global_store_dwordx2 v48, v[34:35], s[30:31] offset:32
	v_mul_f32_e32 v34, v36, v122
	v_mul_f32_e32 v35, v36, v123
	v_cvt_pk_bf16_f32 v34, v34, v35
	v_mul_f32_e32 v35, v36, v124
	v_mul_f32_e32 v37, v36, v125
	v_cvt_pk_bf16_f32 v35, v35, v37
	global_store_dwordx2 v48, v[34:35], s[30:31] offset:48
	v_mul_f32_e32 v34, v36, v94
	v_mul_f32_e32 v35, v36, v95
	v_cvt_pk_bf16_f32 v34, v34, v35
	v_mul_f32_e32 v35, v36, v96
	v_mul_f32_e32 v37, v36, v97
	v_cvt_pk_bf16_f32 v35, v35, v37
	global_store_dwordx2 v48, v[34:35], s[30:31] offset:64
	v_mul_f32_e32 v34, v36, v98
	v_mul_f32_e32 v35, v36, v99
	v_cvt_pk_bf16_f32 v34, v34, v35
	v_mul_f32_e32 v35, v36, v100
	v_mul_f32_e32 v37, v36, v101
	v_cvt_pk_bf16_f32 v35, v35, v37
	global_store_dwordx2 v48, v[34:35], s[30:31] offset:80
	v_mul_f32_e32 v34, v36, v102
	v_mul_f32_e32 v35, v36, v103
	v_cvt_pk_bf16_f32 v34, v34, v35
	v_mul_f32_e32 v35, v36, v104
	v_mul_f32_e32 v37, v36, v105
	v_cvt_pk_bf16_f32 v35, v35, v37
	global_store_dwordx2 v48, v[34:35], s[30:31] offset:96
	v_mul_f32_e32 v34, v36, v106
	v_mul_f32_e32 v35, v36, v107
	v_cvt_pk_bf16_f32 v34, v34, v35
	v_mul_f32_e32 v35, v36, v108
	v_mul_f32_e32 v37, v36, v109
	v_cvt_pk_bf16_f32 v35, v35, v37
	global_store_dwordx2 v48, v[34:35], s[30:31] offset:112
	v_mul_f32_e32 v34, v36, v78
	v_mul_f32_e32 v35, v36, v79
	v_cvt_pk_bf16_f32 v34, v34, v35
	v_mul_f32_e32 v35, v36, v80
	v_mul_f32_e32 v37, v36, v81
	v_cvt_pk_bf16_f32 v35, v35, v37
	global_store_dwordx2 v48, v[34:35], s[30:31] offset:128
	v_mul_f32_e32 v34, v36, v82
	v_mul_f32_e32 v35, v36, v83
	v_cvt_pk_bf16_f32 v34, v34, v35
	v_mul_f32_e32 v35, v36, v84
	v_mul_f32_e32 v37, v36, v85
	v_cvt_pk_bf16_f32 v35, v35, v37
	global_store_dwordx2 v48, v[34:35], s[30:31] offset:144
	v_mul_f32_e32 v34, v36, v86
	v_mul_f32_e32 v35, v36, v87
	v_cvt_pk_bf16_f32 v34, v34, v35
	v_mul_f32_e32 v35, v36, v88
	v_mul_f32_e32 v37, v36, v89
	v_cvt_pk_bf16_f32 v35, v35, v37
	global_store_dwordx2 v48, v[34:35], s[30:31] offset:160
	v_mul_f32_e32 v34, v36, v90
	v_mul_f32_e32 v35, v36, v91
	v_cvt_pk_bf16_f32 v34, v34, v35
	v_mul_f32_e32 v35, v36, v92
	v_mul_f32_e32 v37, v36, v93
	v_cvt_pk_bf16_f32 v35, v35, v37
	global_store_dwordx2 v48, v[34:35], s[30:31] offset:176
	v_mul_f32_e32 v34, v36, v62
	v_mul_f32_e32 v35, v36, v63
	v_cvt_pk_bf16_f32 v34, v34, v35
	v_mul_f32_e32 v35, v36, v64
	v_mul_f32_e32 v37, v36, v65
	v_cvt_pk_bf16_f32 v35, v35, v37
	global_store_dwordx2 v48, v[34:35], s[30:31] offset:192
	v_mul_f32_e32 v34, v36, v66
	v_mul_f32_e32 v35, v36, v67
	v_cvt_pk_bf16_f32 v34, v34, v35
	v_mul_f32_e32 v35, v36, v68
	v_mul_f32_e32 v37, v36, v69
	v_cvt_pk_bf16_f32 v35, v35, v37
	global_store_dwordx2 v48, v[34:35], s[30:31] offset:208
	v_mul_f32_e32 v34, v36, v70
	v_mul_f32_e32 v35, v36, v71
	v_cvt_pk_bf16_f32 v34, v34, v35
	v_mul_f32_e32 v35, v36, v72
	v_mul_f32_e32 v37, v36, v73
	v_cvt_pk_bf16_f32 v35, v35, v37
	global_store_dwordx2 v48, v[34:35], s[30:31] offset:224
	v_mul_f32_e32 v34, v36, v74
	v_mul_f32_e32 v35, v36, v75
	v_cvt_pk_bf16_f32 v34, v34, v35
	v_mul_f32_e32 v35, v36, v76
	v_mul_f32_e32 v36, v36, v77
	v_cvt_pk_bf16_f32 v35, v35, v36
	global_store_dwordx2 v48, v[34:35], s[30:31] offset:240
	v_and_b32_e32 v34, 32, v0
	v_lshl_or_b32 v43, v233, 7, v34
	global_load_dwordx2 v[34:35], v43, s[34:35]
	global_load_dwordx2 v[36:37], v43, s[34:35] offset:64
	global_load_dwordx2 v[98:99], v43, s[34:35] offset:8
	global_load_dwordx2 v[100:101], v43, s[34:35] offset:72
	global_load_dwordx2 v[102:103], v43, s[34:35] offset:16
	global_load_dwordx2 v[104:105], v43, s[34:35] offset:80
	global_load_dwordx2 v[106:107], v43, s[34:35] offset:24
	global_load_dwordx2 v[108:109], v43, s[34:35] offset:88
	v_lshlrev_b32_e32 v39, 16, v126
	v_lshlrev_b32_e32 v38, 16, v130
	s_add_i32 s0, s62, -8
	s_cmp_gt_i32 s62, 8
	s_cselect_b32 s12, s0, 0
	s_sub_i32 s17, s62, s12
	s_add_i32 s17, s17, s16
	s_cmp_gt_i32 s62, -1
	s_cselect_b64 s[0:1], -1, 0
	s_add_i32 s18, s12, s2
	s_and_b64 s[2:3], s[0:1], exec
	s_cselect_b32 s13, s87, s89
	s_cselect_b32 s19, s86, s88
	s_lshl_b32 s14, s18, 6
	s_and_b64 s[2:3], s[0:1], exec
	s_cselect_b32 s14, 0, s14
	s_ashr_i32 s15, s14, 31
	s_mul_i32 s2, s14, 0x2e00
	s_mul_hi_i32 s3, s14, 0x2e00
	s_add_u32 s2, s19, s2
	s_addc_u32 s3, s13, s3
	s_and_b64 s[0:1], s[0:1], exec
	s_cselect_b32 s13, s95, s97
	s_cselect_b32 s19, s94, s96
	s_lshl_b64 s[0:1], s[14:15], 1
	s_add_u32 s0, s19, s0
	s_addc_u32 s1, s13, s1
	s_lshl_b32 s13, s68, 1
	s_or_b32 s13, s13, 1
	s_lshl_b32 s19, s68, 11
	s_lshl_b32 s21, s13, 2
	s_add_i32 s20, s19, 0
	v_mov_b32_e32 v51, v47
	s_lshl_b32 s22, s13, 10
	s_lshl_b32 s23, s68, 4
	v_or_b32_e32 v54, s23, v33
	s_lshl_b32 s24, s13, 3
	v_or_b32_e32 v55, s24, v33
	v_mov_b32_e32 v53, v47
	s_waitcnt vmcnt(7)
; __device__ __forceinline__ unsigned cvt_pk_bf16(float lo, float hi) { unsigned r; asm volatile("v_cvt_pk_bf16_f32 %0, %1, %2" : "=v"(r) : "v"(lo), "v"(hi)); return r; }
; __device__ __forceinline__ gcp uniform_ptr(const void* p) { const unsigned long long v = (unsigned long long)p; const unsigned lo = __builtin_amdgcn_readfirstlane((unsigned)v), hi = __builtin_amdgcn_readfirstlane((unsigned)(v >> 32)); return (gcp)(((unsigned long long)hi << 32) | lo); }
; __device__ __forceinline__ void nsa_unit(const Args& a, LAS unsigned char* lds, int b, int kvh, int qb) {
;     ...
;     { const gcp rpb = uniform_ptr(a.ws + WS_ROPE) + (unsigned)((t * 32 + 8 * h) * 4);
;       u32x4 w0 = __builtin_bit_cast(u32x4, qf[0]), w1 = __builtin_bit_cast(u32x4, qf[1]);
; #pragma unroll
;       for (int jj = 0; jj < 4; ++jj) { const float c0 = gld<float>(rpb + 8 * jj), c1 = gld<float>(rpb + 8 * jj + 4), s0 = gld<float>(rpb + 64 + 8 * jj), s1 = gld<float>(rpb + 64 + 8 * jj + 4);
;           const float xa0 = bflo(w0[jj]), xa1 = bfhi(w0[jj]), xb0 = bflo(w1[jj]), xb1 = bfhi(w1[jj]);
;           w0[jj] = pg8::cvt_pk_bf16(xa0 * c0 - xb0 * s0, xa1 * c1 - xb1 * s1); w1[jj] = pg8::cvt_pk_bf16(xb0 * c0 + xa0 * s0, xb1 * c1 + xa1 * s1); }
;       qf[0] = __builtin_bit_cast(bf16x8, w0); qf[1] = __builtin_bit_cast(bf16x8, w1); }
;     const int nS = qb + 1, jlo = qb > 8 ? qb - 8 : 0, nTot = nS + (qb - jlo + 1);
;     const bf16* ksb = proj + (size_t)b * T * PW + PKS + kvh * 128; const bf16* kwb = proj + (size_t)b * T * PW + PKW + kvh * 128;
;     const bf16* vsb = (const bf16*)(a.ws + WS_VTS) + (size_t)((b * 2 + kvh) * 128) * VTP; const bf16* vwb = (const bf16*)(a.ws + WS_VTW) + (size_t)((b * 2 + kvh) * 128) * VTP;
;     ...
;     const unsigned ldsb = (unsigned)(size_t)lds;
;     constexpr int KRING = 3, VOFF = KRING * NTB;
;     auto tile_src = [&](int i2, const bf16*& kt, const bf16*& vt) { if (i2 < nS) { kt = ksb + (size_t)(64 * i2) * PW; vt = vsb + 64 * i2; } else { const int j = jlo + i2 - nS; kt = kwb + (size_t)(64 * j) * PW; vt = vwb + 64 * j; } };
;     __syncthreads();
;     { const bf16 *kt, *vt; tile_src(0, kt, vt); nsa_dma_tile(kt, PW * 2, vt, VTP * 2, ldsb, ldsb + VOFF, w, lane);
;       if (nTot > 1) { tile_src(1, kt, vt); nsa_dma_tile(kt, PW * 2, vt, VTP * 2, ldsb + NTB, ldsb + VOFF + NTB, w, lane); } }
	v_mov_b32_e32 v41, v34
	s_waitcnt vmcnt(6)
	v_mov_b32_e32 v40, v36
	v_pk_mul_f32 v[40:41], v[40:41], v[38:39]
	s_nop 0
	v_sub_f32_e32 v46, v41, v40
	v_mov_b32_e32 v40, v34
	v_mov_b32_e32 v41, v36
	v_pk_mul_f32 v[38:39], v[40:41], v[38:39]
	v_mov_b32_e32 v34, v37
	v_add_f32_e32 v49, v38, v39
	v_and_b32_e32 v39, 0xffff0000, v126
	v_and_b32_e32 v38, 0xffff0000, v130
	v_pk_mul_f32 v[40:41], v[34:35], v[38:39]
	v_mov_b32_e32 v36, v35
	v_sub_f32_e32 v34, v41, v40
	v_cvt_pk_bf16_f32 v182, v46, v34
	v_pk_mul_f32 v[34:35], v[36:37], v[38:39]
	v_lshlrev_b32_e32 v39, 16, v127
	v_add_f32_e32 v34, v34, v35
	v_cvt_pk_bf16_f32 v186, v49, v34
	s_waitcnt vmcnt(4)
	v_mov_b32_e32 v34, v98
	v_mov_b32_e32 v35, v99
	v_mov_b32_e32 v36, v100
	v_mov_b32_e32 v37, v101
	v_lshlrev_b32_e32 v38, 16, v131
	v_mov_b32_e32 v41, v34
	v_mov_b32_e32 v40, v36
	v_pk_mul_f32 v[40:41], v[40:41], v[38:39]
	s_nop 0
	v_sub_f32_e32 v46, v41, v40
	v_mov_b32_e32 v40, v34
	v_mov_b32_e32 v41, v36
	v_pk_mul_f32 v[38:39], v[40:41], v[38:39]
	v_mov_b32_e32 v34, v37
	v_add_f32_e32 v49, v38, v39
	v_and_b32_e32 v39, 0xffff0000, v127
	v_and_b32_e32 v38, 0xffff0000, v131
	v_pk_mul_f32 v[40:41], v[34:35], v[38:39]
	v_mov_b32_e32 v36, v35
	v_sub_f32_e32 v34, v41, v40
	v_cvt_pk_bf16_f32 v183, v46, v34
	v_pk_mul_f32 v[34:35], v[36:37], v[38:39]
	v_lshlrev_b32_e32 v39, 16, v128
	v_add_f32_e32 v34, v34, v35
	v_cvt_pk_bf16_f32 v187, v49, v34
	s_waitcnt vmcnt(2)
	v_mov_b32_e32 v34, v102
	v_mov_b32_e32 v35, v103
	v_mov_b32_e32 v36, v104
	v_mov_b32_e32 v37, v105
	v_lshlrev_b32_e32 v38, 16, v132
	v_mov_b32_e32 v41, v34
	v_mov_b32_e32 v40, v36
	v_pk_mul_f32 v[40:41], v[40:41], v[38:39]
	s_nop 0
	v_sub_f32_e32 v46, v41, v40
	v_mov_b32_e32 v40, v34
	v_mov_b32_e32 v41, v36
	v_pk_mul_f32 v[38:39], v[40:41], v[38:39]
	v_mov_b32_e32 v34, v37
	v_add_f32_e32 v49, v38, v39
	v_and_b32_e32 v39, 0xffff0000, v128
	v_and_b32_e32 v38, 0xffff0000, v132
	v_pk_mul_f32 v[40:41], v[34:35], v[38:39]
	v_mov_b32_e32 v36, v35
	v_sub_f32_e32 v34, v41, v40
	v_cvt_pk_bf16_f32 v184, v46, v34
	v_pk_mul_f32 v[34:35], v[36:37], v[38:39]
	v_lshlrev_b32_e32 v39, 16, v129
	v_add_f32_e32 v34, v34, v35
	v_cvt_pk_bf16_f32 v188, v49, v34
	s_waitcnt vmcnt(0)
	v_mov_b32_e32 v34, v106
	v_mov_b32_e32 v35, v107
	v_mov_b32_e32 v36, v108
	v_mov_b32_e32 v37, v109
	v_lshlrev_b32_e32 v38, 16, v133
	v_or_b32_e32 v49, s21, v239
	v_mov_b32_e32 v41, v34
	v_mov_b32_e32 v40, v36
	v_pk_mul_f32 v[40:41], v[40:41], v[38:39]
	s_nop 0
	v_sub_f32_e32 v43, v41, v40
	v_mov_b32_e32 v40, v34
	v_mov_b32_e32 v41, v36
	v_pk_mul_f32 v[38:39], v[40:41], v[38:39]
	v_mov_b32_e32 v34, v37
	v_add_f32_e32 v46, v38, v39
	v_and_b32_e32 v39, 0xffff0000, v129
	v_and_b32_e32 v38, 0xffff0000, v133
	v_pk_mul_f32 v[40:41], v[34:35], v[38:39]
	v_mov_b32_e32 v36, v35
	v_sub_f32_e32 v34, v41, v40
	v_cvt_pk_bf16_f32 v185, v43, v34
	v_pk_mul_f32 v[34:35], v[36:37], v[38:39]
	v_or_b32_e32 v43, s63, v239
	v_add_f32_e32 v34, v34, v35
	v_cvt_pk_bf16_f32 v189, v46, v34
	v_bitop3_b32 v34, s63, v0, v239 bitop3:0x36
	v_lshlrev_b32_e32 v34, 4, v34
	v_and_b32_e32 v46, 0xf0, v34
	v_mov_b64_e32 v[34:35], s[2:3]
	v_mad_u64_u32 v[36:37], s[2:3], v43, s73, v[34:35]
	v_lshl_add_u64 v[36:37], v[36:37], 0, v[46:47]
	s_barrier
	s_mov_b32 s2, m0
	s_mov_b32 m0, s20
	s_nop 0
	global_load_lds_dwordx4 v[36:37], off
	s_mov_b32 m0, s2
	v_bitop3_b32 v36, s21, v0, v239 bitop3:0x36
	v_lshlrev_b32_e32 v36, 4, v36
	v_and_b32_e32 v50, 0xf0, v36
	v_mad_u64_u32 v[34:35], s[2:3], v49, s73, v[34:35]
	v_lshl_add_u64 v[34:35], v[34:35], 0, v[50:51]
	s_add_i32 s2, s22, 0
	s_mov_b32 s3, m0
	s_mov_b32 m0, s2
	s_nop 0
	global_load_lds_dwordx4 v[34:35], off
	s_mov_b32 m0, s3
	v_mov_b64_e32 v[34:35], s[0:1]
	v_mad_u64_u32 v[36:37], s[0:1], v54, s74, v[34:35]
	v_lshl_add_u64 v[36:37], v[36:37], 0, v[230:231]
	s_add_i32 s0, s19, s75
	s_mov_b32 s1, m0
	s_mov_b32 m0, s0
	s_nop 0
	global_load_lds_dwordx4 v[36:37], off
	s_mov_b32 m0, s1
	v_lshrrev_b32_e32 v36, 1, v55
	v_xor_b32_e32 v36, v36, v0
	v_lshlrev_b32_e32 v36, 4, v36
	v_and_b32_e32 v52, 0x70, v36
	v_mad_u64_u32 v[34:35], s[0:1], v55, s74, v[34:35]
	v_lshl_add_u64 v[34:35], v[34:35], 0, v[52:53]
	s_add_i32 s0, s22, s75
	s_mov_b32 s1, m0
	s_mov_b32 m0, s0
	s_nop 0
	global_load_lds_dwordx4 v[34:35], off
	s_mov_b32 m0, s1
	s_cmp_lt_i32 s17, 1
	s_cbranch_scc1 .LBB0_1838
	v_mad_u64_u32 v[34:35], s[0:1], v43, s73, 0
	v_mad_u64_u32 v[36:37], s[0:1], v49, s73, 0
	v_mad_u64_u32 v[38:39], s[0:1], v54, s74, 0
	v_mad_u64_u32 v[40:41], s[0:1], v55, s74, 0
	s_cmp_gt_i32 s62, 0
	s_cselect_b64 s[0:1], -1, 0
	s_sub_i32 s12, s12, s62
	s_and_b64 s[2:3], s[0:1], exec
	s_cselect_b32 s13, s87, s89
	s_cselect_b32 s14, s86, s88
	s_lshl_b32 s12, s12, 6
	s_and_b64 s[2:3], s[0:1], exec
	s_cselect_b32 s2, 64, s12
	s_ashr_i32 s3, s2, 31
	s_mul_i32 s12, s2, 0x2e00
	s_mul_hi_i32 s15, s2, 0x2e00
	s_add_u32 s12, s14, s12
	s_addc_u32 s13, s13, s15
	s_and_b64 s[0:1], s[0:1], exec
	s_cselect_b32 s14, s95, s97
	s_cselect_b32 s15, s94, s96
	s_lshl_b64 s[0:1], s[2:3], 1
	s_add_u32 s0, s15, s0
	v_lshl_add_u64 v[34:35], s[12:13], 0, v[34:35]
	s_addc_u32 s1, s14, s1
	v_lshl_add_u64 v[34:35], v[34:35], 0, v[46:47]
	s_add_i32 s2, 0, 0x4000
	s_add_i32 s3, s19, s2
	s_mov_b32 s14, m0
	s_mov_b32 m0, s3
	s_nop 0
	global_load_lds_dwordx4 v[34:35], off
	s_mov_b32 m0, s14
	v_lshl_add_u64 v[34:35], s[12:13], 0, v[36:37]
	v_lshl_add_u64 v[34:35], v[34:35], 0, v[50:51]
	s_add_i32 s2, s22, s2
	s_mov_b32 s3, m0
	s_mov_b32 m0, s2
	s_nop 0
	global_load_lds_dwordx4 v[34:35], off
	s_mov_b32 m0, s3
	v_lshl_add_u64 v[34:35], s[0:1], 0, v[38:39]
	v_lshl_add_u64 v[34:35], v[34:35], 0, v[230:231]
	s_add_i32 s2, 0, 0x10000
	s_add_i32 s3, s19, s2
	s_mov_b32 s12, m0
	s_mov_b32 m0, s3
	s_nop 0
	global_load_lds_dwordx4 v[34:35], off
	s_mov_b32 m0, s12
	v_lshl_add_u64 v[34:35], s[0:1], 0, v[40:41]
	v_lshl_add_u64 v[34:35], v[34:35], 0, v[52:53]
	s_add_i32 s0, s22, s2
	s_mov_b32 s1, m0
	s_mov_b32 m0, s0
	s_nop 0
	global_load_lds_dwordx4 v[34:35], off
	s_mov_b32 m0, s1
